# v026
# speedup vs baseline: 1.1062x; 1.0021x over previous
.LBB2_45:
	s_and_b64 vcc, exec, s[28:29]
	s_cbranch_vccnz .Lmy_epi_last
	s_cmp_eq_u32 s30, 7
	s_cbranch_scc1 .Lmy_epi_nl7
	v_exp_f32_e32 v120, v120
	v_exp_f32_e32 v121, v121
	v_exp_f32_e32 v122, v122
	v_pk_add_f32 v[120:121], v[120:121], 1.0 op_sel_hi:[1,0]
	v_exp_f32_e32 v123, v123
	v_exp_f32_e32 v124, v124
	v_pk_add_f32 v[122:123], v[122:123], 1.0 op_sel_hi:[1,0]
	v_exp_f32_e32 v125, v125
	v_exp_f32_e32 v126, v126
	v_pk_add_f32 v[124:125], v[124:125], 1.0 op_sel_hi:[1,0]
	v_exp_f32_e32 v127, v127
	v_exp_f32_e32 v116, v116
	v_pk_add_f32 v[126:127], v[126:127], 1.0 op_sel_hi:[1,0]
	v_exp_f32_e32 v117, v117
	v_pk_mul_f32 v[120:121], v[120:121], v[124:125]
	v_exp_f32_e32 v118, v118
	v_pk_mul_f32 v[122:123], v[122:123], v[126:127]
	v_exp_f32_e32 v119, v119
	v_pk_add_f32 v[124:125], v[124:125], 2.0 op_sel_hi:[1,0] neg_lo:[1,0] neg_hi:[1,0]
	v_pk_add_f32 v[116:117], v[116:117], 1.0 op_sel_hi:[1,0]
	v_pk_add_f32 v[126:127], v[126:127], 2.0 op_sel_hi:[1,0] neg_lo:[1,0] neg_hi:[1,0]
	v_pk_add_f32 v[118:119], v[118:119], 1.0 op_sel_hi:[1,0]
	v_pk_mul_f32 v[124:125], v[124:125], v[116:117]
	v_pk_mul_f32 v[116:117], v[116:117], v[120:121]
	v_pk_mul_f32 v[126:127], v[126:127], v[118:119]
	v_pk_mul_f32 v[118:119], v[118:119], v[122:123]
	v_rcp_f32_e32 v116, v116
	v_rcp_f32_e32 v117, v117
	v_rcp_f32_e32 v118, v118
	v_rcp_f32_e32 v119, v119
	s_waitcnt lgkmcnt(3)
	v_pk_fma_f32 v[124:125], v[172:173], v[120:121], v[124:125]
	v_pk_fma_f32 v[126:127], v[174:175], v[122:123], v[126:127]
	v_pk_mul_f32 v[116:117], v[116:117], v[124:125]
	v_pk_mul_f32 v[118:119], v[118:119], v[126:127]
	global_store_dwordx4 v[176:177], v[116:119], off nt
	s_nop 1
	v_pk_mul_f32 v[116:117], v[116:117], s[96:97] op_sel_hi:[1,0]
	v_pk_mul_f32 v[118:119], v[118:119], s[96:97] op_sel_hi:[1,0]
	v_exp_f32_e32 v112, v112
	v_exp_f32_e32 v113, v113
	v_exp_f32_e32 v114, v114
	v_pk_fma_f32 v[112:113], v[112:113], s[98:99], s[98:99] op_sel_hi:[1,0,0]
	v_exp_f32_e32 v115, v115
	v_exp_f32_e32 v116, v116
	v_pk_fma_f32 v[114:115], v[114:115], s[98:99], s[98:99] op_sel_hi:[1,0,0]
	v_exp_f32_e32 v117, v117
	v_exp_f32_e32 v118, v118
	v_pk_add_f32 v[116:117], v[116:117], 1.0 op_sel_hi:[1,0]
	v_exp_f32_e32 v119, v119
	v_pk_mul_f32 v[112:113], v[112:113], v[116:117]
	v_rcp_f32_e32 v112, v112
	v_pk_add_f32 v[118:119], v[118:119], 1.0 op_sel_hi:[1,0]
	v_rcp_f32_e32 v113, v113
	v_pk_mul_f32 v[114:115], v[114:115], v[118:119]
	v_pk_add_f32 v[116:117], v[116:117], 2.0 op_sel_hi:[1,0] neg_lo:[1,0] neg_hi:[1,0]
	v_rcp_f32_e32 v114, v114
	v_rcp_f32_e32 v115, v115
	v_pk_add_f32 v[118:119], v[118:119], 2.0 op_sel_hi:[1,0] neg_lo:[1,0] neg_hi:[1,0]
	v_pk_mul_f32 v[112:113], v[112:113], v[116:117]
	v_pk_mul_f32 v[114:115], v[114:115], v[118:119]
	v_cvt_pk_fp8_f32 v124, v112, v113
	s_add_u32 s0, s8, s27
	s_addc_u32 s1, s9, 0
	s_ashr_i32 s35, s34, 31
	s_lshl_b64 s[34:35], s[34:35], 21
	v_ashrrev_i32_e32 v209, 31, v208
	s_add_u32 s36, s73, s34
	v_lshl_add_u64 v[122:123], s[0:1], 0, v[210:211]
	v_cvt_pk_fp8_f32 v124, v114, v115 op_sel:[0,0,1]
	v_lshlrev_b64 v[116:117], 10, v[208:209]
	s_addc_u32 s37, s74, s35
	v_lshl_add_u64 v[118:119], v[122:123], 0, v[116:117]
	global_store_dword v[118:119], v124, off
	s_cmp_eq_u32 s30, 7
	s_cselect_b64 s[34:35], -1, 0
	s_cmp_lg_u32 s30, 7
	v_lshl_add_u64 v[120:121], v[210:211], 1, s[36:37]
	v_exp_f32_e32 v104, v104
	v_exp_f32_e32 v105, v105
	v_exp_f32_e32 v106, v106
	v_pk_add_f32 v[104:105], v[104:105], 1.0 op_sel_hi:[1,0]
	v_exp_f32_e32 v107, v107
	v_exp_f32_e32 v108, v108
	v_pk_add_f32 v[106:107], v[106:107], 1.0 op_sel_hi:[1,0]
	v_exp_f32_e32 v109, v109
	v_exp_f32_e32 v110, v110
	v_pk_add_f32 v[108:109], v[108:109], 1.0 op_sel_hi:[1,0]
	v_exp_f32_e32 v111, v111
	v_exp_f32_e32 v100, v100
	v_pk_add_f32 v[110:111], v[110:111], 1.0 op_sel_hi:[1,0]
	v_exp_f32_e32 v101, v101
	v_pk_mul_f32 v[104:105], v[104:105], v[108:109]
	v_exp_f32_e32 v102, v102
	v_pk_mul_f32 v[106:107], v[106:107], v[110:111]
	v_exp_f32_e32 v103, v103
	v_pk_add_f32 v[108:109], v[108:109], 2.0 op_sel_hi:[1,0] neg_lo:[1,0] neg_hi:[1,0]
	v_pk_add_f32 v[100:101], v[100:101], 1.0 op_sel_hi:[1,0]
	v_pk_add_f32 v[110:111], v[110:111], 2.0 op_sel_hi:[1,0] neg_lo:[1,0] neg_hi:[1,0]
	v_pk_add_f32 v[102:103], v[102:103], 1.0 op_sel_hi:[1,0]
	v_pk_mul_f32 v[108:109], v[108:109], v[100:101]
	v_pk_mul_f32 v[100:101], v[100:101], v[104:105]
	v_pk_mul_f32 v[110:111], v[110:111], v[102:103]
	v_pk_mul_f32 v[102:103], v[102:103], v[106:107]
	v_rcp_f32_e32 v100, v100
	v_rcp_f32_e32 v101, v101
	v_rcp_f32_e32 v102, v102
	v_rcp_f32_e32 v103, v103
	s_waitcnt lgkmcnt(2)
	v_pk_fma_f32 v[108:109], v[168:169], v[104:105], v[108:109]
	v_pk_fma_f32 v[110:111], v[170:171], v[106:107], v[110:111]
	v_lshl_add_u64 v[104:105], v[176:177], 0, s[18:19]
	v_pk_mul_f32 v[100:101], v[100:101], v[108:109]
	v_pk_mul_f32 v[102:103], v[102:103], v[110:111]
	global_store_dwordx4 v[104:105], v[100:103], off nt
	s_nop 1
	v_pk_mul_f32 v[100:101], v[100:101], s[96:97] op_sel_hi:[1,0]
	v_pk_mul_f32 v[102:103], v[102:103], s[96:97] op_sel_hi:[1,0]
	v_exp_f32_e32 v96, v96
	v_exp_f32_e32 v97, v97
	v_exp_f32_e32 v98, v98
	v_pk_fma_f32 v[96:97], v[96:97], s[98:99], s[98:99] op_sel_hi:[1,0,0]
	v_exp_f32_e32 v99, v99
	v_exp_f32_e32 v100, v100
	v_pk_fma_f32 v[98:99], v[98:99], s[98:99], s[98:99] op_sel_hi:[1,0,0]
	v_exp_f32_e32 v101, v101
	v_exp_f32_e32 v102, v102
	v_pk_add_f32 v[100:101], v[100:101], 1.0 op_sel_hi:[1,0]
	v_exp_f32_e32 v103, v103
	v_pk_mul_f32 v[96:97], v[96:97], v[100:101]
	v_rcp_f32_e32 v96, v96
	v_pk_add_f32 v[102:103], v[102:103], 1.0 op_sel_hi:[1,0]
	v_rcp_f32_e32 v97, v97
	v_pk_mul_f32 v[98:99], v[98:99], v[102:103]
	v_pk_add_f32 v[100:101], v[100:101], 2.0 op_sel_hi:[1,0] neg_lo:[1,0] neg_hi:[1,0]
	v_rcp_f32_e32 v98, v98
	v_rcp_f32_e32 v99, v99
	v_pk_add_f32 v[102:103], v[102:103], 2.0 op_sel_hi:[1,0] neg_lo:[1,0] neg_hi:[1,0]
	v_pk_mul_f32 v[96:97], v[96:97], v[100:101]
	v_pk_mul_f32 v[98:99], v[98:99], v[102:103]
	v_cvt_pk_fp8_f32 v104, v96, v97
	v_ashrrev_i32_e32 v207, 31, v206
	v_lshlrev_b64 v[100:101], 10, v[206:207]
	v_lshl_add_u64 v[102:103], v[122:123], 0, v[100:101]
	v_cvt_pk_fp8_f32 v104, v98, v99 op_sel:[0,0,1]
	v_cndmask_b32_e64 v105, 0, 1, s[34:35]
	global_store_dword v[102:103], v104, off
	v_cmp_ne_u32_e64 s[0:1], 1, v105
	v_exp_f32_e32 v88, v88
	v_exp_f32_e32 v89, v89
	v_exp_f32_e32 v90, v90
	v_pk_add_f32 v[88:89], v[88:89], 1.0 op_sel_hi:[1,0]
	v_exp_f32_e32 v91, v91
	v_exp_f32_e32 v92, v92
	v_pk_add_f32 v[90:91], v[90:91], 1.0 op_sel_hi:[1,0]
	v_exp_f32_e32 v93, v93
	v_exp_f32_e32 v94, v94
	v_pk_add_f32 v[92:93], v[92:93], 1.0 op_sel_hi:[1,0]
	v_exp_f32_e32 v95, v95
	v_exp_f32_e32 v84, v84
	v_pk_add_f32 v[94:95], v[94:95], 1.0 op_sel_hi:[1,0]
	v_exp_f32_e32 v85, v85
	v_pk_mul_f32 v[88:89], v[88:89], v[92:93]
	v_exp_f32_e32 v86, v86
	v_pk_mul_f32 v[90:91], v[90:91], v[94:95]
	v_exp_f32_e32 v87, v87
	v_pk_add_f32 v[92:93], v[92:93], 2.0 op_sel_hi:[1,0] neg_lo:[1,0] neg_hi:[1,0]
	v_pk_add_f32 v[84:85], v[84:85], 1.0 op_sel_hi:[1,0]
	v_pk_add_f32 v[94:95], v[94:95], 2.0 op_sel_hi:[1,0] neg_lo:[1,0] neg_hi:[1,0]
	v_pk_add_f32 v[86:87], v[86:87], 1.0 op_sel_hi:[1,0]
	v_pk_mul_f32 v[92:93], v[92:93], v[84:85]
	v_pk_mul_f32 v[84:85], v[84:85], v[88:89]
	v_pk_mul_f32 v[94:95], v[94:95], v[86:87]
	v_pk_mul_f32 v[86:87], v[86:87], v[90:91]
	v_rcp_f32_e32 v84, v84
	v_rcp_f32_e32 v85, v85
	v_rcp_f32_e32 v86, v86
	v_rcp_f32_e32 v87, v87
	s_waitcnt lgkmcnt(1)
	v_pk_fma_f32 v[92:93], v[164:165], v[88:89], v[92:93]
	v_pk_fma_f32 v[94:95], v[166:167], v[90:91], v[94:95]
	v_pk_mul_f32 v[84:85], v[84:85], v[92:93]
	v_pk_mul_f32 v[86:87], v[86:87], v[94:95]
	v_lshl_add_u64 v[88:89], v[176:177], 0, s[12:13]
	global_store_dwordx4 v[88:89], v[84:87], off nt
	s_nop 1
	v_pk_mul_f32 v[84:85], v[84:85], s[96:97] op_sel_hi:[1,0]
	v_pk_mul_f32 v[86:87], v[86:87], s[96:97] op_sel_hi:[1,0]
	v_exp_f32_e32 v80, v80
	v_exp_f32_e32 v81, v81
	v_exp_f32_e32 v82, v82
	v_pk_fma_f32 v[80:81], v[80:81], s[98:99], s[98:99] op_sel_hi:[1,0,0]
	v_exp_f32_e32 v83, v83
	v_exp_f32_e32 v84, v84
	v_pk_fma_f32 v[82:83], v[82:83], s[98:99], s[98:99] op_sel_hi:[1,0,0]
	v_exp_f32_e32 v85, v85
	v_exp_f32_e32 v86, v86
	v_pk_add_f32 v[84:85], v[84:85], 1.0 op_sel_hi:[1,0]
	v_exp_f32_e32 v87, v87
	v_pk_mul_f32 v[80:81], v[80:81], v[84:85]
	v_rcp_f32_e32 v80, v80
	v_pk_add_f32 v[86:87], v[86:87], 1.0 op_sel_hi:[1,0]
	v_rcp_f32_e32 v81, v81
	v_pk_mul_f32 v[82:83], v[82:83], v[86:87]
	v_pk_add_f32 v[84:85], v[84:85], 2.0 op_sel_hi:[1,0] neg_lo:[1,0] neg_hi:[1,0]
	v_rcp_f32_e32 v82, v82
	v_rcp_f32_e32 v83, v83
	v_pk_add_f32 v[86:87], v[86:87], 2.0 op_sel_hi:[1,0] neg_lo:[1,0] neg_hi:[1,0]
	v_pk_mul_f32 v[80:81], v[80:81], v[84:85]
	v_pk_mul_f32 v[82:83], v[82:83], v[86:87]
	v_ashrrev_i32_e32 v205, 31, v204
	v_cvt_pk_fp8_f32 v88, v80, v81
	s_and_b64 vcc, exec, s[0:1]
	v_cvt_pk_fp8_f32 v88, v82, v83 op_sel:[0,0,1]
	v_lshlrev_b64 v[84:85], 10, v[204:205]
	v_lshl_add_u64 v[86:87], v[122:123], 0, v[84:85]
	global_store_dword v[86:87], v88, off
	v_exp_f32_e32 v72, v72
	v_exp_f32_e32 v73, v73
	v_exp_f32_e32 v74, v74
	v_pk_add_f32 v[72:73], v[72:73], 1.0 op_sel_hi:[1,0]
	v_exp_f32_e32 v75, v75
	v_exp_f32_e32 v76, v76
	v_pk_add_f32 v[74:75], v[74:75], 1.0 op_sel_hi:[1,0]
	v_exp_f32_e32 v77, v77
	v_exp_f32_e32 v78, v78
	v_pk_add_f32 v[76:77], v[76:77], 1.0 op_sel_hi:[1,0]
	v_exp_f32_e32 v79, v79
	v_exp_f32_e32 v68, v68
	v_pk_add_f32 v[78:79], v[78:79], 1.0 op_sel_hi:[1,0]
	v_exp_f32_e32 v69, v69
	v_pk_mul_f32 v[72:73], v[72:73], v[76:77]
	v_exp_f32_e32 v70, v70
	v_pk_mul_f32 v[74:75], v[74:75], v[78:79]
	v_exp_f32_e32 v71, v71
	v_pk_add_f32 v[76:77], v[76:77], 2.0 op_sel_hi:[1,0] neg_lo:[1,0] neg_hi:[1,0]
	v_pk_add_f32 v[68:69], v[68:69], 1.0 op_sel_hi:[1,0]
	v_pk_add_f32 v[78:79], v[78:79], 2.0 op_sel_hi:[1,0] neg_lo:[1,0] neg_hi:[1,0]
	v_pk_add_f32 v[70:71], v[70:71], 1.0 op_sel_hi:[1,0]
	v_pk_mul_f32 v[76:77], v[76:77], v[68:69]
	v_pk_mul_f32 v[68:69], v[68:69], v[72:73]
	v_pk_mul_f32 v[78:79], v[78:79], v[70:71]
	v_pk_mul_f32 v[70:71], v[70:71], v[74:75]
	v_rcp_f32_e32 v68, v68
	v_rcp_f32_e32 v69, v69
	v_rcp_f32_e32 v70, v70
	v_rcp_f32_e32 v71, v71
	s_waitcnt lgkmcnt(0)
	v_pk_fma_f32 v[76:77], v[160:161], v[72:73], v[76:77]
	v_pk_fma_f32 v[78:79], v[162:163], v[74:75], v[78:79]
	v_lshl_add_u64 v[72:73], v[176:177], 0, s[20:21]
	v_pk_mul_f32 v[68:69], v[68:69], v[76:77]
	v_pk_mul_f32 v[70:71], v[70:71], v[78:79]
	global_store_dwordx4 v[72:73], v[68:71], off nt
	s_nop 1
	v_pk_mul_f32 v[68:69], v[68:69], s[96:97] op_sel_hi:[1,0]
	v_pk_mul_f32 v[70:71], v[70:71], s[96:97] op_sel_hi:[1,0]
	v_exp_f32_e32 v64, v64
	v_exp_f32_e32 v65, v65
	v_exp_f32_e32 v66, v66
	v_pk_fma_f32 v[64:65], v[64:65], s[98:99], s[98:99] op_sel_hi:[1,0,0]
	v_exp_f32_e32 v67, v67
	v_exp_f32_e32 v68, v68
	v_pk_fma_f32 v[66:67], v[66:67], s[98:99], s[98:99] op_sel_hi:[1,0,0]
	v_exp_f32_e32 v69, v69
	v_exp_f32_e32 v70, v70
	v_pk_add_f32 v[68:69], v[68:69], 1.0 op_sel_hi:[1,0]
	v_exp_f32_e32 v71, v71
	v_pk_mul_f32 v[64:65], v[64:65], v[68:69]
	v_rcp_f32_e32 v64, v64
	v_pk_add_f32 v[70:71], v[70:71], 1.0 op_sel_hi:[1,0]
	v_rcp_f32_e32 v65, v65
	v_pk_mul_f32 v[66:67], v[66:67], v[70:71]
	v_pk_add_f32 v[68:69], v[68:69], 2.0 op_sel_hi:[1,0] neg_lo:[1,0] neg_hi:[1,0]
	v_rcp_f32_e32 v66, v66
	v_rcp_f32_e32 v67, v67
	v_pk_add_f32 v[70:71], v[70:71], 2.0 op_sel_hi:[1,0] neg_lo:[1,0] neg_hi:[1,0]
	v_pk_mul_f32 v[64:65], v[64:65], v[68:69]
	v_pk_mul_f32 v[66:67], v[66:67], v[70:71]
	v_ashrrev_i32_e32 v203, 31, v202
	v_cvt_pk_fp8_f32 v72, v64, v65
	s_and_b64 vcc, exec, s[0:1]
	v_cvt_pk_fp8_f32 v72, v66, v67 op_sel:[0,0,1]
	v_lshlrev_b64 v[68:69], 10, v[202:203]
	v_lshl_add_u64 v[70:71], v[122:123], 0, v[68:69]
	global_store_dword v[70:71], v72, off
	v_exp_f32_e32 v56, v56
	v_exp_f32_e32 v57, v57
	v_exp_f32_e32 v58, v58
	v_pk_add_f32 v[56:57], v[56:57], 1.0 op_sel_hi:[1,0]
	v_exp_f32_e32 v59, v59
	v_exp_f32_e32 v60, v60
	v_pk_add_f32 v[58:59], v[58:59], 1.0 op_sel_hi:[1,0]
	v_exp_f32_e32 v61, v61
	v_exp_f32_e32 v62, v62
	v_pk_add_f32 v[60:61], v[60:61], 1.0 op_sel_hi:[1,0]
	v_exp_f32_e32 v63, v63
	v_exp_f32_e32 v52, v52
	v_pk_add_f32 v[62:63], v[62:63], 1.0 op_sel_hi:[1,0]
	v_exp_f32_e32 v53, v53
	v_pk_mul_f32 v[56:57], v[56:57], v[60:61]
	v_exp_f32_e32 v54, v54
	v_pk_mul_f32 v[58:59], v[58:59], v[62:63]
	v_exp_f32_e32 v55, v55
	v_pk_add_f32 v[60:61], v[60:61], 2.0 op_sel_hi:[1,0] neg_lo:[1,0] neg_hi:[1,0]
	v_pk_add_f32 v[52:53], v[52:53], 1.0 op_sel_hi:[1,0]
	v_pk_add_f32 v[62:63], v[62:63], 2.0 op_sel_hi:[1,0] neg_lo:[1,0] neg_hi:[1,0]
	v_pk_add_f32 v[54:55], v[54:55], 1.0 op_sel_hi:[1,0]
	v_pk_mul_f32 v[60:61], v[60:61], v[52:53]
	v_pk_mul_f32 v[52:53], v[52:53], v[56:57]
	v_pk_mul_f32 v[62:63], v[62:63], v[54:55]
	v_pk_mul_f32 v[54:55], v[54:55], v[58:59]
	v_rcp_f32_e32 v52, v52
	v_rcp_f32_e32 v53, v53
	v_rcp_f32_e32 v54, v54
	v_rcp_f32_e32 v55, v55
	s_waitcnt vmcnt(8)
	v_pk_fma_f32 v[60:61], v[156:157], v[56:57], v[60:61]
	v_pk_fma_f32 v[62:63], v[158:159], v[58:59], v[62:63]
	v_pk_mul_f32 v[52:53], v[52:53], v[60:61]
	v_pk_mul_f32 v[54:55], v[54:55], v[62:63]
	v_lshl_add_u64 v[56:57], v[176:177], 0, s[14:15]
	global_store_dwordx4 v[56:57], v[52:55], off nt
	s_nop 1
	v_pk_mul_f32 v[52:53], v[52:53], s[96:97] op_sel_hi:[1,0]
	v_pk_mul_f32 v[54:55], v[54:55], s[96:97] op_sel_hi:[1,0]
	v_exp_f32_e32 v48, v48
	v_exp_f32_e32 v49, v49
	v_exp_f32_e32 v50, v50
	v_pk_fma_f32 v[48:49], v[48:49], s[98:99], s[98:99] op_sel_hi:[1,0,0]
	v_exp_f32_e32 v51, v51
	v_exp_f32_e32 v52, v52
	v_pk_fma_f32 v[50:51], v[50:51], s[98:99], s[98:99] op_sel_hi:[1,0,0]
	v_exp_f32_e32 v53, v53
	v_exp_f32_e32 v54, v54
	v_pk_add_f32 v[52:53], v[52:53], 1.0 op_sel_hi:[1,0]
	v_exp_f32_e32 v55, v55
	v_pk_mul_f32 v[48:49], v[48:49], v[52:53]
	v_rcp_f32_e32 v48, v48
	v_pk_add_f32 v[54:55], v[54:55], 1.0 op_sel_hi:[1,0]
	v_rcp_f32_e32 v49, v49
	v_pk_mul_f32 v[50:51], v[50:51], v[54:55]
	v_pk_add_f32 v[52:53], v[52:53], 2.0 op_sel_hi:[1,0] neg_lo:[1,0] neg_hi:[1,0]
	v_rcp_f32_e32 v50, v50
	v_rcp_f32_e32 v51, v51
	v_pk_add_f32 v[54:55], v[54:55], 2.0 op_sel_hi:[1,0] neg_lo:[1,0] neg_hi:[1,0]
	v_pk_mul_f32 v[48:49], v[48:49], v[52:53]
	v_pk_mul_f32 v[50:51], v[50:51], v[54:55]
	v_ashrrev_i32_e32 v201, 31, v200
	v_cvt_pk_fp8_f32 v56, v48, v49
	s_and_b64 vcc, exec, s[0:1]
	v_cvt_pk_fp8_f32 v56, v50, v51 op_sel:[0,0,1]
	v_lshlrev_b64 v[52:53], 10, v[200:201]
	v_lshl_add_u64 v[54:55], v[122:123], 0, v[52:53]
	global_store_dword v[54:55], v56, off
	v_exp_f32_e32 v40, v40
	v_exp_f32_e32 v41, v41
	v_exp_f32_e32 v42, v42
	v_pk_add_f32 v[40:41], v[40:41], 1.0 op_sel_hi:[1,0]
	v_exp_f32_e32 v43, v43
	v_exp_f32_e32 v44, v44
	v_pk_add_f32 v[42:43], v[42:43], 1.0 op_sel_hi:[1,0]
	v_exp_f32_e32 v45, v45
	v_exp_f32_e32 v46, v46
	v_pk_add_f32 v[44:45], v[44:45], 1.0 op_sel_hi:[1,0]
	v_exp_f32_e32 v47, v47
	v_exp_f32_e32 v36, v36
	v_pk_add_f32 v[46:47], v[46:47], 1.0 op_sel_hi:[1,0]
	v_exp_f32_e32 v37, v37
	v_pk_mul_f32 v[40:41], v[40:41], v[44:45]
	v_exp_f32_e32 v38, v38
	v_pk_mul_f32 v[42:43], v[42:43], v[46:47]
	v_exp_f32_e32 v39, v39
	v_pk_add_f32 v[44:45], v[44:45], 2.0 op_sel_hi:[1,0] neg_lo:[1,0] neg_hi:[1,0]
	v_pk_add_f32 v[36:37], v[36:37], 1.0 op_sel_hi:[1,0]
	v_pk_add_f32 v[46:47], v[46:47], 2.0 op_sel_hi:[1,0] neg_lo:[1,0] neg_hi:[1,0]
	v_pk_add_f32 v[38:39], v[38:39], 1.0 op_sel_hi:[1,0]
	v_pk_mul_f32 v[44:45], v[44:45], v[36:37]
	v_pk_mul_f32 v[36:37], v[36:37], v[40:41]
	v_pk_mul_f32 v[46:47], v[46:47], v[38:39]
	v_pk_mul_f32 v[38:39], v[38:39], v[42:43]
	v_rcp_f32_e32 v36, v36
	v_rcp_f32_e32 v37, v37
	v_rcp_f32_e32 v38, v38
	v_rcp_f32_e32 v39, v39
	v_pk_fma_f32 v[44:45], v[152:153], v[40:41], v[44:45]
	v_pk_fma_f32 v[46:47], v[154:155], v[42:43], v[46:47]
	v_lshl_add_u64 v[40:41], v[176:177], 0, s[22:23]
	v_pk_mul_f32 v[36:37], v[36:37], v[44:45]
	v_pk_mul_f32 v[38:39], v[38:39], v[46:47]
	global_store_dwordx4 v[40:41], v[36:39], off nt
	s_nop 1
	v_pk_mul_f32 v[36:37], v[36:37], s[96:97] op_sel_hi:[1,0]
	v_pk_mul_f32 v[38:39], v[38:39], s[96:97] op_sel_hi:[1,0]
	v_exp_f32_e32 v32, v32
	v_exp_f32_e32 v33, v33
	v_exp_f32_e32 v34, v34
	v_pk_fma_f32 v[32:33], v[32:33], s[98:99], s[98:99] op_sel_hi:[1,0,0]
	v_exp_f32_e32 v35, v35
	v_exp_f32_e32 v36, v36
	v_pk_fma_f32 v[34:35], v[34:35], s[98:99], s[98:99] op_sel_hi:[1,0,0]
	v_exp_f32_e32 v37, v37
	v_exp_f32_e32 v38, v38
	v_pk_add_f32 v[36:37], v[36:37], 1.0 op_sel_hi:[1,0]
	v_exp_f32_e32 v39, v39
	v_pk_mul_f32 v[32:33], v[32:33], v[36:37]
	v_rcp_f32_e32 v32, v32
	v_pk_add_f32 v[38:39], v[38:39], 1.0 op_sel_hi:[1,0]
	v_rcp_f32_e32 v33, v33
	v_pk_mul_f32 v[34:35], v[34:35], v[38:39]
	v_pk_add_f32 v[36:37], v[36:37], 2.0 op_sel_hi:[1,0] neg_lo:[1,0] neg_hi:[1,0]
	v_rcp_f32_e32 v34, v34
	v_rcp_f32_e32 v35, v35
	v_pk_add_f32 v[38:39], v[38:39], 2.0 op_sel_hi:[1,0] neg_lo:[1,0] neg_hi:[1,0]
	v_pk_mul_f32 v[32:33], v[32:33], v[36:37]
	v_pk_mul_f32 v[34:35], v[34:35], v[38:39]
	v_cvt_pk_fp8_f32 v40, v32, v33
	v_or_b32_e32 v36, 16, v200
	v_ashrrev_i32_e32 v37, 31, v36
	v_lshlrev_b64 v[36:37], 10, v[36:37]
	v_cvt_pk_fp8_f32 v40, v34, v35 op_sel:[0,0,1]
	v_lshl_add_u64 v[38:39], v[122:123], 0, v[36:37]
	global_store_dword v[38:39], v40, off
	v_exp_f32_e32 v24, v24
	v_exp_f32_e32 v25, v25
	v_exp_f32_e32 v26, v26
	v_pk_add_f32 v[24:25], v[24:25], 1.0 op_sel_hi:[1,0]
	v_exp_f32_e32 v27, v27
	v_exp_f32_e32 v28, v28
	v_pk_add_f32 v[26:27], v[26:27], 1.0 op_sel_hi:[1,0]
	v_exp_f32_e32 v29, v29
	v_exp_f32_e32 v30, v30
	v_pk_add_f32 v[28:29], v[28:29], 1.0 op_sel_hi:[1,0]
	v_exp_f32_e32 v31, v31
	v_exp_f32_e32 v20, v20
	v_pk_add_f32 v[30:31], v[30:31], 1.0 op_sel_hi:[1,0]
	v_exp_f32_e32 v21, v21
	v_pk_mul_f32 v[24:25], v[24:25], v[28:29]
	v_exp_f32_e32 v22, v22
	v_pk_mul_f32 v[26:27], v[26:27], v[30:31]
	v_exp_f32_e32 v23, v23
	v_pk_add_f32 v[28:29], v[28:29], 2.0 op_sel_hi:[1,0] neg_lo:[1,0] neg_hi:[1,0]
	v_pk_add_f32 v[20:21], v[20:21], 1.0 op_sel_hi:[1,0]
	v_pk_add_f32 v[30:31], v[30:31], 2.0 op_sel_hi:[1,0] neg_lo:[1,0] neg_hi:[1,0]
	v_pk_add_f32 v[22:23], v[22:23], 1.0 op_sel_hi:[1,0]
	v_pk_mul_f32 v[28:29], v[28:29], v[20:21]
	v_pk_mul_f32 v[20:21], v[20:21], v[24:25]
	v_pk_mul_f32 v[30:31], v[30:31], v[22:23]
	v_pk_mul_f32 v[22:23], v[22:23], v[26:27]
	v_rcp_f32_e32 v20, v20
	v_rcp_f32_e32 v21, v21
	v_rcp_f32_e32 v22, v22
	v_rcp_f32_e32 v23, v23
	v_pk_fma_f32 v[28:29], v[148:149], v[24:25], v[28:29]
	v_pk_fma_f32 v[30:31], v[150:151], v[26:27], v[30:31]
	v_pk_mul_f32 v[20:21], v[20:21], v[28:29]
	v_pk_mul_f32 v[22:23], v[22:23], v[30:31]
	v_lshl_add_u64 v[24:25], v[176:177], 0, s[16:17]
	global_store_dwordx4 v[24:25], v[20:23], off nt
	s_nop 1
	v_pk_mul_f32 v[20:21], v[20:21], s[96:97] op_sel_hi:[1,0]
	v_pk_mul_f32 v[22:23], v[22:23], s[96:97] op_sel_hi:[1,0]
	v_exp_f32_e32 v16, v16
	v_exp_f32_e32 v17, v17
	v_exp_f32_e32 v18, v18
	v_pk_fma_f32 v[16:17], v[16:17], s[98:99], s[98:99] op_sel_hi:[1,0,0]
	v_exp_f32_e32 v19, v19
	v_exp_f32_e32 v20, v20
	v_pk_fma_f32 v[18:19], v[18:19], s[98:99], s[98:99] op_sel_hi:[1,0,0]
	v_exp_f32_e32 v21, v21
	v_exp_f32_e32 v22, v22
	v_pk_add_f32 v[20:21], v[20:21], 1.0 op_sel_hi:[1,0]
	v_exp_f32_e32 v23, v23
	v_pk_mul_f32 v[16:17], v[16:17], v[20:21]
	v_rcp_f32_e32 v16, v16
	v_pk_add_f32 v[22:23], v[22:23], 1.0 op_sel_hi:[1,0]
	v_rcp_f32_e32 v17, v17
	v_pk_mul_f32 v[18:19], v[18:19], v[22:23]
	v_pk_add_f32 v[20:21], v[20:21], 2.0 op_sel_hi:[1,0] neg_lo:[1,0] neg_hi:[1,0]
	v_rcp_f32_e32 v18, v18
	v_rcp_f32_e32 v19, v19
	v_pk_add_f32 v[22:23], v[22:23], 2.0 op_sel_hi:[1,0] neg_lo:[1,0] neg_hi:[1,0]
	v_pk_mul_f32 v[16:17], v[16:17], v[20:21]
	v_pk_mul_f32 v[18:19], v[18:19], v[22:23]
	v_cvt_pk_fp8_f32 v24, v16, v17
	v_or_b32_e32 v20, 32, v200
	v_ashrrev_i32_e32 v21, 31, v20
	v_lshlrev_b64 v[20:21], 10, v[20:21]
	v_cvt_pk_fp8_f32 v24, v18, v19 op_sel:[0,0,1]
	v_lshl_add_u64 v[22:23], v[122:123], 0, v[20:21]
	global_store_dword v[22:23], v24, off
	v_exp_f32_e32 v8, v8
	v_exp_f32_e32 v9, v9
	v_exp_f32_e32 v10, v10
	v_pk_add_f32 v[8:9], v[8:9], 1.0 op_sel_hi:[1,0]
	v_exp_f32_e32 v11, v11
	v_exp_f32_e32 v12, v12
	v_pk_add_f32 v[10:11], v[10:11], 1.0 op_sel_hi:[1,0]
	v_exp_f32_e32 v13, v13
	v_exp_f32_e32 v14, v14
	v_pk_add_f32 v[12:13], v[12:13], 1.0 op_sel_hi:[1,0]
	v_exp_f32_e32 v15, v15
	v_exp_f32_e32 v4, v4
	v_pk_add_f32 v[14:15], v[14:15], 1.0 op_sel_hi:[1,0]
	v_exp_f32_e32 v5, v5
	v_pk_mul_f32 v[8:9], v[8:9], v[12:13]
	v_exp_f32_e32 v6, v6
	v_pk_mul_f32 v[10:11], v[10:11], v[14:15]
	v_exp_f32_e32 v7, v7
	v_pk_add_f32 v[12:13], v[12:13], 2.0 op_sel_hi:[1,0] neg_lo:[1,0] neg_hi:[1,0]
	v_pk_add_f32 v[4:5], v[4:5], 1.0 op_sel_hi:[1,0]
	v_pk_add_f32 v[14:15], v[14:15], 2.0 op_sel_hi:[1,0] neg_lo:[1,0] neg_hi:[1,0]
	v_pk_add_f32 v[6:7], v[6:7], 1.0 op_sel_hi:[1,0]
	v_pk_mul_f32 v[12:13], v[12:13], v[4:5]
	v_pk_mul_f32 v[4:5], v[4:5], v[8:9]
	v_pk_mul_f32 v[14:15], v[14:15], v[6:7]
	v_pk_mul_f32 v[6:7], v[6:7], v[10:11]
	v_rcp_f32_e32 v4, v4
	v_rcp_f32_e32 v5, v5
	v_rcp_f32_e32 v6, v6
	v_rcp_f32_e32 v7, v7
	v_pk_fma_f32 v[12:13], v[144:145], v[8:9], v[12:13]
	v_pk_fma_f32 v[14:15], v[146:147], v[10:11], v[14:15]
	v_lshl_add_u64 v[8:9], v[176:177], 0, s[24:25]
	v_pk_mul_f32 v[4:5], v[4:5], v[12:13]
	v_pk_mul_f32 v[6:7], v[6:7], v[14:15]
	global_store_dwordx4 v[8:9], v[4:7], off nt
	s_nop 1
	v_pk_mul_f32 v[4:5], v[4:5], s[96:97] op_sel_hi:[1,0]
	v_pk_mul_f32 v[6:7], v[6:7], s[96:97] op_sel_hi:[1,0]
	v_exp_f32_e32 v0, v0
	v_exp_f32_e32 v1, v1
	v_exp_f32_e32 v2, v2
	v_pk_fma_f32 v[0:1], v[0:1], s[98:99], s[98:99] op_sel_hi:[1,0,0]
	v_exp_f32_e32 v3, v3
	v_exp_f32_e32 v4, v4
	v_pk_fma_f32 v[2:3], v[2:3], s[98:99], s[98:99] op_sel_hi:[1,0,0]
	v_exp_f32_e32 v5, v5
	v_exp_f32_e32 v6, v6
	v_pk_add_f32 v[4:5], v[4:5], 1.0 op_sel_hi:[1,0]
	v_exp_f32_e32 v7, v7
	v_pk_mul_f32 v[0:1], v[0:1], v[4:5]
	v_rcp_f32_e32 v0, v0
	v_pk_add_f32 v[6:7], v[6:7], 1.0 op_sel_hi:[1,0]
	v_rcp_f32_e32 v1, v1
	v_pk_mul_f32 v[2:3], v[2:3], v[6:7]
	v_pk_add_f32 v[4:5], v[4:5], 2.0 op_sel_hi:[1,0] neg_lo:[1,0] neg_hi:[1,0]
	v_rcp_f32_e32 v2, v2
	v_rcp_f32_e32 v3, v3
	v_pk_add_f32 v[6:7], v[6:7], 2.0 op_sel_hi:[1,0] neg_lo:[1,0] neg_hi:[1,0]
	v_pk_mul_f32 v[0:1], v[0:1], v[4:5]
	v_pk_mul_f32 v[2:3], v[2:3], v[6:7]
	v_cvt_pk_fp8_f32 v8, v0, v1
	v_or_b32_e32 v4, 48, v200
	v_ashrrev_i32_e32 v5, 31, v4
	v_lshlrev_b64 v[4:5], 10, v[4:5]
	v_cvt_pk_fp8_f32 v8, v2, v3 op_sel:[0,0,1]
	v_lshl_add_u64 v[6:7], v[122:123], 0, v[4:5]
	global_store_dword v[6:7], v8, off
	s_branch .LBB2_24
.Lmy_epi_nl7:
	v_exp_f32_e32 v120, v120
	v_exp_f32_e32 v121, v121
	v_exp_f32_e32 v122, v122
	v_pk_add_f32 v[120:121], v[120:121], 1.0 op_sel_hi:[1,0]
	v_exp_f32_e32 v123, v123
	v_exp_f32_e32 v124, v124
	v_pk_add_f32 v[122:123], v[122:123], 1.0 op_sel_hi:[1,0]
	v_exp_f32_e32 v125, v125
	v_exp_f32_e32 v126, v126
	v_pk_add_f32 v[124:125], v[124:125], 1.0 op_sel_hi:[1,0]
	v_exp_f32_e32 v127, v127
	v_exp_f32_e32 v116, v116
	v_pk_add_f32 v[126:127], v[126:127], 1.0 op_sel_hi:[1,0]
	v_exp_f32_e32 v117, v117
	v_pk_mul_f32 v[120:121], v[120:121], v[124:125]
	v_exp_f32_e32 v118, v118
	v_pk_mul_f32 v[122:123], v[122:123], v[126:127]
	v_exp_f32_e32 v119, v119
	v_pk_add_f32 v[124:125], v[124:125], 2.0 op_sel_hi:[1,0] neg_lo:[1,0] neg_hi:[1,0]
	v_pk_add_f32 v[116:117], v[116:117], 1.0 op_sel_hi:[1,0]
	v_pk_add_f32 v[126:127], v[126:127], 2.0 op_sel_hi:[1,0] neg_lo:[1,0] neg_hi:[1,0]
	v_pk_add_f32 v[118:119], v[118:119], 1.0 op_sel_hi:[1,0]
	v_pk_mul_f32 v[124:125], v[124:125], v[116:117]
	v_pk_mul_f32 v[116:117], v[116:117], v[120:121]
	v_pk_mul_f32 v[126:127], v[126:127], v[118:119]
	v_pk_mul_f32 v[118:119], v[118:119], v[122:123]
	v_rcp_f32_e32 v116, v116
	v_rcp_f32_e32 v117, v117
	v_rcp_f32_e32 v118, v118
	v_rcp_f32_e32 v119, v119
	s_waitcnt lgkmcnt(3)
	v_pk_fma_f32 v[124:125], v[172:173], v[120:121], v[124:125]
	v_pk_fma_f32 v[126:127], v[174:175], v[122:123], v[126:127]
	v_pk_mul_f32 v[116:117], v[116:117], v[124:125]
	v_pk_mul_f32 v[118:119], v[118:119], v[126:127]
	global_store_dwordx4 v[176:177], v[116:119], off nt
	s_nop 1
	v_pk_mul_f32 v[116:117], v[116:117], s[96:97] op_sel_hi:[1,0]
	v_pk_mul_f32 v[118:119], v[118:119], s[96:97] op_sel_hi:[1,0]
	v_exp_f32_e32 v112, v112
	v_exp_f32_e32 v113, v113
	v_exp_f32_e32 v114, v114
	v_pk_fma_f32 v[112:113], v[112:113], s[98:99], s[98:99] op_sel_hi:[1,0,0]
	v_exp_f32_e32 v115, v115
	v_exp_f32_e32 v116, v116
	v_pk_fma_f32 v[114:115], v[114:115], s[98:99], s[98:99] op_sel_hi:[1,0,0]
	v_exp_f32_e32 v117, v117
	v_exp_f32_e32 v118, v118
	v_pk_add_f32 v[116:117], v[116:117], 1.0 op_sel_hi:[1,0]
	v_exp_f32_e32 v119, v119
	v_pk_mul_f32 v[112:113], v[112:113], v[116:117]
	v_rcp_f32_e32 v112, v112
	v_pk_add_f32 v[118:119], v[118:119], 1.0 op_sel_hi:[1,0]
	v_rcp_f32_e32 v113, v113
	v_pk_mul_f32 v[114:115], v[114:115], v[118:119]
	v_pk_add_f32 v[116:117], v[116:117], 2.0 op_sel_hi:[1,0] neg_lo:[1,0] neg_hi:[1,0]
	v_rcp_f32_e32 v114, v114
	v_rcp_f32_e32 v115, v115
	v_pk_add_f32 v[118:119], v[118:119], 2.0 op_sel_hi:[1,0] neg_lo:[1,0] neg_hi:[1,0]
	v_pk_mul_f32 v[112:113], v[112:113], v[116:117]
	v_pk_mul_f32 v[114:115], v[114:115], v[118:119]
	v_cvt_pk_fp8_f32 v124, v112, v113
	s_add_u32 s0, s8, s27
	s_addc_u32 s1, s9, 0
	s_ashr_i32 s35, s34, 31
	s_lshl_b64 s[34:35], s[34:35], 21
	v_ashrrev_i32_e32 v209, 31, v208
	s_add_u32 s36, s73, s34
	v_lshl_add_u64 v[122:123], s[0:1], 0, v[210:211]
	v_cvt_pk_fp8_f32 v124, v114, v115 op_sel:[0,0,1]
	v_lshlrev_b64 v[116:117], 10, v[208:209]
	s_addc_u32 s37, s74, s35
	v_lshl_add_u64 v[118:119], v[122:123], 0, v[116:117]
	global_store_dword v[118:119], v124, off
	s_cmp_eq_u32 s30, 7
	s_cselect_b64 s[34:35], -1, 0
	s_cmp_lg_u32 s30, 7
	v_lshl_add_u64 v[120:121], v[210:211], 1, s[36:37]
	v_pk_mul_f32 v[112:113], v[112:113], s[98:99] op_sel_hi:[1,0]
	v_pk_mul_f32 v[114:115], v[114:115], s[98:99] op_sel_hi:[1,0]
	v_cvt_pk_f16_f32 v112, v112, v113
	v_cvt_pk_f16_f32 v113, v114, v115
	v_lshl_add_u64 v[114:115], v[116:117], 1, v[120:121]
	global_store_dwordx2 v[114:115], v[112:113], off
	v_exp_f32_e32 v104, v104
	v_exp_f32_e32 v105, v105
	v_exp_f32_e32 v106, v106
	v_pk_add_f32 v[104:105], v[104:105], 1.0 op_sel_hi:[1,0]
	v_exp_f32_e32 v107, v107
	v_exp_f32_e32 v108, v108
	v_pk_add_f32 v[106:107], v[106:107], 1.0 op_sel_hi:[1,0]
	v_exp_f32_e32 v109, v109
	v_exp_f32_e32 v110, v110
	v_pk_add_f32 v[108:109], v[108:109], 1.0 op_sel_hi:[1,0]
	v_exp_f32_e32 v111, v111
	v_exp_f32_e32 v100, v100
	v_pk_add_f32 v[110:111], v[110:111], 1.0 op_sel_hi:[1,0]
	v_exp_f32_e32 v101, v101
	v_pk_mul_f32 v[104:105], v[104:105], v[108:109]
	v_exp_f32_e32 v102, v102
	v_pk_mul_f32 v[106:107], v[106:107], v[110:111]
	v_exp_f32_e32 v103, v103
	v_pk_add_f32 v[108:109], v[108:109], 2.0 op_sel_hi:[1,0] neg_lo:[1,0] neg_hi:[1,0]
	v_pk_add_f32 v[100:101], v[100:101], 1.0 op_sel_hi:[1,0]
	v_pk_add_f32 v[110:111], v[110:111], 2.0 op_sel_hi:[1,0] neg_lo:[1,0] neg_hi:[1,0]
	v_pk_add_f32 v[102:103], v[102:103], 1.0 op_sel_hi:[1,0]
	v_pk_mul_f32 v[108:109], v[108:109], v[100:101]
	v_pk_mul_f32 v[100:101], v[100:101], v[104:105]
	v_pk_mul_f32 v[110:111], v[110:111], v[102:103]
	v_pk_mul_f32 v[102:103], v[102:103], v[106:107]
	v_rcp_f32_e32 v100, v100
	v_rcp_f32_e32 v101, v101
	v_rcp_f32_e32 v102, v102
	v_rcp_f32_e32 v103, v103
	s_waitcnt lgkmcnt(2)
	v_pk_fma_f32 v[108:109], v[168:169], v[104:105], v[108:109]
	v_pk_fma_f32 v[110:111], v[170:171], v[106:107], v[110:111]
	v_lshl_add_u64 v[104:105], v[176:177], 0, s[18:19]
	v_pk_mul_f32 v[100:101], v[100:101], v[108:109]
	v_pk_mul_f32 v[102:103], v[102:103], v[110:111]
	global_store_dwordx4 v[104:105], v[100:103], off nt
	s_nop 1
	v_pk_mul_f32 v[100:101], v[100:101], s[96:97] op_sel_hi:[1,0]
	v_pk_mul_f32 v[102:103], v[102:103], s[96:97] op_sel_hi:[1,0]
	v_exp_f32_e32 v96, v96
	v_exp_f32_e32 v97, v97
	v_exp_f32_e32 v98, v98
	v_pk_fma_f32 v[96:97], v[96:97], s[98:99], s[98:99] op_sel_hi:[1,0,0]
	v_exp_f32_e32 v99, v99
	v_exp_f32_e32 v100, v100
	v_pk_fma_f32 v[98:99], v[98:99], s[98:99], s[98:99] op_sel_hi:[1,0,0]
	v_exp_f32_e32 v101, v101
	v_exp_f32_e32 v102, v102
	v_pk_add_f32 v[100:101], v[100:101], 1.0 op_sel_hi:[1,0]
	v_exp_f32_e32 v103, v103
	v_pk_mul_f32 v[96:97], v[96:97], v[100:101]
	v_rcp_f32_e32 v96, v96
	v_pk_add_f32 v[102:103], v[102:103], 1.0 op_sel_hi:[1,0]
	v_rcp_f32_e32 v97, v97
	v_pk_mul_f32 v[98:99], v[98:99], v[102:103]
	v_pk_add_f32 v[100:101], v[100:101], 2.0 op_sel_hi:[1,0] neg_lo:[1,0] neg_hi:[1,0]
	v_rcp_f32_e32 v98, v98
	v_rcp_f32_e32 v99, v99
	v_pk_add_f32 v[102:103], v[102:103], 2.0 op_sel_hi:[1,0] neg_lo:[1,0] neg_hi:[1,0]
	v_pk_mul_f32 v[96:97], v[96:97], v[100:101]
	v_pk_mul_f32 v[98:99], v[98:99], v[102:103]
	v_cvt_pk_fp8_f32 v104, v96, v97
	v_ashrrev_i32_e32 v207, 31, v206
	v_lshlrev_b64 v[100:101], 10, v[206:207]
	v_lshl_add_u64 v[102:103], v[122:123], 0, v[100:101]
	v_cvt_pk_fp8_f32 v104, v98, v99 op_sel:[0,0,1]
	v_cndmask_b32_e64 v105, 0, 1, s[34:35]
	global_store_dword v[102:103], v104, off
	v_cmp_ne_u32_e64 s[0:1], 1, v105
	v_pk_mul_f32 v[96:97], v[96:97], s[98:99] op_sel_hi:[1,0]
	v_pk_mul_f32 v[98:99], v[98:99], s[98:99] op_sel_hi:[1,0]
	v_cvt_pk_f16_f32 v96, v96, v97
	v_cvt_pk_f16_f32 v97, v98, v99
	v_lshl_add_u64 v[98:99], v[100:101], 1, v[120:121]
	global_store_dwordx2 v[98:99], v[96:97], off
	v_exp_f32_e32 v88, v88
	v_exp_f32_e32 v89, v89
	v_exp_f32_e32 v90, v90
	v_pk_add_f32 v[88:89], v[88:89], 1.0 op_sel_hi:[1,0]
	v_exp_f32_e32 v91, v91
	v_exp_f32_e32 v92, v92
	v_pk_add_f32 v[90:91], v[90:91], 1.0 op_sel_hi:[1,0]
	v_exp_f32_e32 v93, v93
	v_exp_f32_e32 v94, v94
	v_pk_add_f32 v[92:93], v[92:93], 1.0 op_sel_hi:[1,0]
	v_exp_f32_e32 v95, v95
	v_exp_f32_e32 v84, v84
	v_pk_add_f32 v[94:95], v[94:95], 1.0 op_sel_hi:[1,0]
	v_exp_f32_e32 v85, v85
	v_pk_mul_f32 v[88:89], v[88:89], v[92:93]
	v_exp_f32_e32 v86, v86
	v_pk_mul_f32 v[90:91], v[90:91], v[94:95]
	v_exp_f32_e32 v87, v87
	v_pk_add_f32 v[92:93], v[92:93], 2.0 op_sel_hi:[1,0] neg_lo:[1,0] neg_hi:[1,0]
	v_pk_add_f32 v[84:85], v[84:85], 1.0 op_sel_hi:[1,0]
	v_pk_add_f32 v[94:95], v[94:95], 2.0 op_sel_hi:[1,0] neg_lo:[1,0] neg_hi:[1,0]
	v_pk_add_f32 v[86:87], v[86:87], 1.0 op_sel_hi:[1,0]
	v_pk_mul_f32 v[92:93], v[92:93], v[84:85]
	v_pk_mul_f32 v[84:85], v[84:85], v[88:89]
	v_pk_mul_f32 v[94:95], v[94:95], v[86:87]
	v_pk_mul_f32 v[86:87], v[86:87], v[90:91]
	v_rcp_f32_e32 v84, v84
	v_rcp_f32_e32 v85, v85
	v_rcp_f32_e32 v86, v86
	v_rcp_f32_e32 v87, v87
	s_waitcnt lgkmcnt(1)
	v_pk_fma_f32 v[92:93], v[164:165], v[88:89], v[92:93]
	v_pk_fma_f32 v[94:95], v[166:167], v[90:91], v[94:95]
	v_pk_mul_f32 v[84:85], v[84:85], v[92:93]
	v_pk_mul_f32 v[86:87], v[86:87], v[94:95]
	v_lshl_add_u64 v[88:89], v[176:177], 0, s[12:13]
	global_store_dwordx4 v[88:89], v[84:87], off nt
	s_nop 1
	v_pk_mul_f32 v[84:85], v[84:85], s[96:97] op_sel_hi:[1,0]
	v_pk_mul_f32 v[86:87], v[86:87], s[96:97] op_sel_hi:[1,0]
	v_exp_f32_e32 v80, v80
	v_exp_f32_e32 v81, v81
	v_exp_f32_e32 v82, v82
	v_pk_fma_f32 v[80:81], v[80:81], s[98:99], s[98:99] op_sel_hi:[1,0,0]
	v_exp_f32_e32 v83, v83
	v_exp_f32_e32 v84, v84
	v_pk_fma_f32 v[82:83], v[82:83], s[98:99], s[98:99] op_sel_hi:[1,0,0]
	v_exp_f32_e32 v85, v85
	v_exp_f32_e32 v86, v86
	v_pk_add_f32 v[84:85], v[84:85], 1.0 op_sel_hi:[1,0]
	v_exp_f32_e32 v87, v87
	v_pk_mul_f32 v[80:81], v[80:81], v[84:85]
	v_rcp_f32_e32 v80, v80
	v_pk_add_f32 v[86:87], v[86:87], 1.0 op_sel_hi:[1,0]
	v_rcp_f32_e32 v81, v81
	v_pk_mul_f32 v[82:83], v[82:83], v[86:87]
	v_pk_add_f32 v[84:85], v[84:85], 2.0 op_sel_hi:[1,0] neg_lo:[1,0] neg_hi:[1,0]
	v_rcp_f32_e32 v82, v82
	v_rcp_f32_e32 v83, v83
	v_pk_add_f32 v[86:87], v[86:87], 2.0 op_sel_hi:[1,0] neg_lo:[1,0] neg_hi:[1,0]
	v_pk_mul_f32 v[80:81], v[80:81], v[84:85]
	v_pk_mul_f32 v[82:83], v[82:83], v[86:87]
	v_ashrrev_i32_e32 v205, 31, v204
	v_cvt_pk_fp8_f32 v88, v80, v81
	s_and_b64 vcc, exec, s[0:1]
	v_cvt_pk_fp8_f32 v88, v82, v83 op_sel:[0,0,1]
	v_lshlrev_b64 v[84:85], 10, v[204:205]
	v_lshl_add_u64 v[86:87], v[122:123], 0, v[84:85]
	global_store_dword v[86:87], v88, off
	v_pk_mul_f32 v[80:81], v[80:81], s[98:99] op_sel_hi:[1,0]
	v_pk_mul_f32 v[82:83], v[82:83], s[98:99] op_sel_hi:[1,0]
	v_cvt_pk_f16_f32 v80, v80, v81
	v_cvt_pk_f16_f32 v81, v82, v83
	v_lshl_add_u64 v[82:83], v[84:85], 1, v[120:121]
	global_store_dwordx2 v[82:83], v[80:81], off
	v_exp_f32_e32 v72, v72
	v_exp_f32_e32 v73, v73
	v_exp_f32_e32 v74, v74
	v_pk_add_f32 v[72:73], v[72:73], 1.0 op_sel_hi:[1,0]
	v_exp_f32_e32 v75, v75
	v_exp_f32_e32 v76, v76
	v_pk_add_f32 v[74:75], v[74:75], 1.0 op_sel_hi:[1,0]
	v_exp_f32_e32 v77, v77
	v_exp_f32_e32 v78, v78
	v_pk_add_f32 v[76:77], v[76:77], 1.0 op_sel_hi:[1,0]
	v_exp_f32_e32 v79, v79
	v_exp_f32_e32 v68, v68
	v_pk_add_f32 v[78:79], v[78:79], 1.0 op_sel_hi:[1,0]
	v_exp_f32_e32 v69, v69
	v_pk_mul_f32 v[72:73], v[72:73], v[76:77]
	v_exp_f32_e32 v70, v70
	v_pk_mul_f32 v[74:75], v[74:75], v[78:79]
	v_exp_f32_e32 v71, v71
	v_pk_add_f32 v[76:77], v[76:77], 2.0 op_sel_hi:[1,0] neg_lo:[1,0] neg_hi:[1,0]
	v_pk_add_f32 v[68:69], v[68:69], 1.0 op_sel_hi:[1,0]
	v_pk_add_f32 v[78:79], v[78:79], 2.0 op_sel_hi:[1,0] neg_lo:[1,0] neg_hi:[1,0]
	v_pk_add_f32 v[70:71], v[70:71], 1.0 op_sel_hi:[1,0]
	v_pk_mul_f32 v[76:77], v[76:77], v[68:69]
	v_pk_mul_f32 v[68:69], v[68:69], v[72:73]
	v_pk_mul_f32 v[78:79], v[78:79], v[70:71]
	v_pk_mul_f32 v[70:71], v[70:71], v[74:75]
	v_rcp_f32_e32 v68, v68
	v_rcp_f32_e32 v69, v69
	v_rcp_f32_e32 v70, v70
	v_rcp_f32_e32 v71, v71
	s_waitcnt lgkmcnt(0)
	v_pk_fma_f32 v[76:77], v[160:161], v[72:73], v[76:77]
	v_pk_fma_f32 v[78:79], v[162:163], v[74:75], v[78:79]
	v_lshl_add_u64 v[72:73], v[176:177], 0, s[20:21]
	v_pk_mul_f32 v[68:69], v[68:69], v[76:77]
	v_pk_mul_f32 v[70:71], v[70:71], v[78:79]
	global_store_dwordx4 v[72:73], v[68:71], off nt
	s_nop 1
	v_pk_mul_f32 v[68:69], v[68:69], s[96:97] op_sel_hi:[1,0]
	v_pk_mul_f32 v[70:71], v[70:71], s[96:97] op_sel_hi:[1,0]
	v_exp_f32_e32 v64, v64
	v_exp_f32_e32 v65, v65
	v_exp_f32_e32 v66, v66
	v_pk_fma_f32 v[64:65], v[64:65], s[98:99], s[98:99] op_sel_hi:[1,0,0]
	v_exp_f32_e32 v67, v67
	v_exp_f32_e32 v68, v68
	v_pk_fma_f32 v[66:67], v[66:67], s[98:99], s[98:99] op_sel_hi:[1,0,0]
	v_exp_f32_e32 v69, v69
	v_exp_f32_e32 v70, v70
	v_pk_add_f32 v[68:69], v[68:69], 1.0 op_sel_hi:[1,0]
	v_exp_f32_e32 v71, v71
	v_pk_mul_f32 v[64:65], v[64:65], v[68:69]
	v_rcp_f32_e32 v64, v64
	v_pk_add_f32 v[70:71], v[70:71], 1.0 op_sel_hi:[1,0]
	v_rcp_f32_e32 v65, v65
	v_pk_mul_f32 v[66:67], v[66:67], v[70:71]
	v_pk_add_f32 v[68:69], v[68:69], 2.0 op_sel_hi:[1,0] neg_lo:[1,0] neg_hi:[1,0]
	v_rcp_f32_e32 v66, v66
	v_rcp_f32_e32 v67, v67
	v_pk_add_f32 v[70:71], v[70:71], 2.0 op_sel_hi:[1,0] neg_lo:[1,0] neg_hi:[1,0]
	v_pk_mul_f32 v[64:65], v[64:65], v[68:69]
	v_pk_mul_f32 v[66:67], v[66:67], v[70:71]
	v_ashrrev_i32_e32 v203, 31, v202
	v_cvt_pk_fp8_f32 v72, v64, v65
	s_and_b64 vcc, exec, s[0:1]
	v_cvt_pk_fp8_f32 v72, v66, v67 op_sel:[0,0,1]
	v_lshlrev_b64 v[68:69], 10, v[202:203]
	v_lshl_add_u64 v[70:71], v[122:123], 0, v[68:69]
	global_store_dword v[70:71], v72, off
	v_pk_mul_f32 v[64:65], v[64:65], s[98:99] op_sel_hi:[1,0]
	v_pk_mul_f32 v[66:67], v[66:67], s[98:99] op_sel_hi:[1,0]
	v_cvt_pk_f16_f32 v64, v64, v65
	v_cvt_pk_f16_f32 v65, v66, v67
	v_lshl_add_u64 v[66:67], v[68:69], 1, v[120:121]
	global_store_dwordx2 v[66:67], v[64:65], off
	v_exp_f32_e32 v56, v56
	v_exp_f32_e32 v57, v57
	v_exp_f32_e32 v58, v58
	v_pk_add_f32 v[56:57], v[56:57], 1.0 op_sel_hi:[1,0]
	v_exp_f32_e32 v59, v59
	v_exp_f32_e32 v60, v60
	v_pk_add_f32 v[58:59], v[58:59], 1.0 op_sel_hi:[1,0]
	v_exp_f32_e32 v61, v61
	v_exp_f32_e32 v62, v62
	v_pk_add_f32 v[60:61], v[60:61], 1.0 op_sel_hi:[1,0]
	v_exp_f32_e32 v63, v63
	v_exp_f32_e32 v52, v52
	v_pk_add_f32 v[62:63], v[62:63], 1.0 op_sel_hi:[1,0]
	v_exp_f32_e32 v53, v53
	v_pk_mul_f32 v[56:57], v[56:57], v[60:61]
	v_exp_f32_e32 v54, v54
	v_pk_mul_f32 v[58:59], v[58:59], v[62:63]
	v_exp_f32_e32 v55, v55
	v_pk_add_f32 v[60:61], v[60:61], 2.0 op_sel_hi:[1,0] neg_lo:[1,0] neg_hi:[1,0]
	v_pk_add_f32 v[52:53], v[52:53], 1.0 op_sel_hi:[1,0]
	v_pk_add_f32 v[62:63], v[62:63], 2.0 op_sel_hi:[1,0] neg_lo:[1,0] neg_hi:[1,0]
	v_pk_add_f32 v[54:55], v[54:55], 1.0 op_sel_hi:[1,0]
	v_pk_mul_f32 v[60:61], v[60:61], v[52:53]
	v_pk_mul_f32 v[52:53], v[52:53], v[56:57]
	v_pk_mul_f32 v[62:63], v[62:63], v[54:55]
	v_pk_mul_f32 v[54:55], v[54:55], v[58:59]
	v_rcp_f32_e32 v52, v52
	v_rcp_f32_e32 v53, v53
	v_rcp_f32_e32 v54, v54
	v_rcp_f32_e32 v55, v55
	s_waitcnt vmcnt(8)
	v_pk_fma_f32 v[60:61], v[156:157], v[56:57], v[60:61]
	v_pk_fma_f32 v[62:63], v[158:159], v[58:59], v[62:63]
	v_pk_mul_f32 v[52:53], v[52:53], v[60:61]
	v_pk_mul_f32 v[54:55], v[54:55], v[62:63]
	v_lshl_add_u64 v[56:57], v[176:177], 0, s[14:15]
	global_store_dwordx4 v[56:57], v[52:55], off nt
	s_nop 1
	v_pk_mul_f32 v[52:53], v[52:53], s[96:97] op_sel_hi:[1,0]
	v_pk_mul_f32 v[54:55], v[54:55], s[96:97] op_sel_hi:[1,0]
	v_exp_f32_e32 v48, v48
	v_exp_f32_e32 v49, v49
	v_exp_f32_e32 v50, v50
	v_pk_fma_f32 v[48:49], v[48:49], s[98:99], s[98:99] op_sel_hi:[1,0,0]
	v_exp_f32_e32 v51, v51
	v_exp_f32_e32 v52, v52
	v_pk_fma_f32 v[50:51], v[50:51], s[98:99], s[98:99] op_sel_hi:[1,0,0]
	v_exp_f32_e32 v53, v53
	v_exp_f32_e32 v54, v54
	v_pk_add_f32 v[52:53], v[52:53], 1.0 op_sel_hi:[1,0]
	v_exp_f32_e32 v55, v55
	v_pk_mul_f32 v[48:49], v[48:49], v[52:53]
	v_rcp_f32_e32 v48, v48
	v_pk_add_f32 v[54:55], v[54:55], 1.0 op_sel_hi:[1,0]
	v_rcp_f32_e32 v49, v49
	v_pk_mul_f32 v[50:51], v[50:51], v[54:55]
	v_pk_add_f32 v[52:53], v[52:53], 2.0 op_sel_hi:[1,0] neg_lo:[1,0] neg_hi:[1,0]
	v_rcp_f32_e32 v50, v50
	v_rcp_f32_e32 v51, v51
	v_pk_add_f32 v[54:55], v[54:55], 2.0 op_sel_hi:[1,0] neg_lo:[1,0] neg_hi:[1,0]
	v_pk_mul_f32 v[48:49], v[48:49], v[52:53]
	v_pk_mul_f32 v[50:51], v[50:51], v[54:55]
	v_ashrrev_i32_e32 v201, 31, v200
	v_cvt_pk_fp8_f32 v56, v48, v49
	s_and_b64 vcc, exec, s[0:1]
	v_cvt_pk_fp8_f32 v56, v50, v51 op_sel:[0,0,1]
	v_lshlrev_b64 v[52:53], 10, v[200:201]
	v_lshl_add_u64 v[54:55], v[122:123], 0, v[52:53]
	global_store_dword v[54:55], v56, off
	v_pk_mul_f32 v[48:49], v[48:49], s[98:99] op_sel_hi:[1,0]
	v_pk_mul_f32 v[50:51], v[50:51], s[98:99] op_sel_hi:[1,0]
	v_cvt_pk_f16_f32 v48, v48, v49
	v_cvt_pk_f16_f32 v49, v50, v51
	v_lshl_add_u64 v[50:51], v[52:53], 1, v[120:121]
	global_store_dwordx2 v[50:51], v[48:49], off
	v_exp_f32_e32 v40, v40
	v_exp_f32_e32 v41, v41
	v_exp_f32_e32 v42, v42
	v_pk_add_f32 v[40:41], v[40:41], 1.0 op_sel_hi:[1,0]
	v_exp_f32_e32 v43, v43
	v_exp_f32_e32 v44, v44
	v_pk_add_f32 v[42:43], v[42:43], 1.0 op_sel_hi:[1,0]
	v_exp_f32_e32 v45, v45
	v_exp_f32_e32 v46, v46
	v_pk_add_f32 v[44:45], v[44:45], 1.0 op_sel_hi:[1,0]
	v_exp_f32_e32 v47, v47
	v_exp_f32_e32 v36, v36
	v_pk_add_f32 v[46:47], v[46:47], 1.0 op_sel_hi:[1,0]
	v_exp_f32_e32 v37, v37
	v_pk_mul_f32 v[40:41], v[40:41], v[44:45]
	v_exp_f32_e32 v38, v38
	v_pk_mul_f32 v[42:43], v[42:43], v[46:47]
	v_exp_f32_e32 v39, v39
	v_pk_add_f32 v[44:45], v[44:45], 2.0 op_sel_hi:[1,0] neg_lo:[1,0] neg_hi:[1,0]
	v_pk_add_f32 v[36:37], v[36:37], 1.0 op_sel_hi:[1,0]
	v_pk_add_f32 v[46:47], v[46:47], 2.0 op_sel_hi:[1,0] neg_lo:[1,0] neg_hi:[1,0]
	v_pk_add_f32 v[38:39], v[38:39], 1.0 op_sel_hi:[1,0]
	v_pk_mul_f32 v[44:45], v[44:45], v[36:37]
	v_pk_mul_f32 v[36:37], v[36:37], v[40:41]
	v_pk_mul_f32 v[46:47], v[46:47], v[38:39]
	v_pk_mul_f32 v[38:39], v[38:39], v[42:43]
	v_rcp_f32_e32 v36, v36
	v_rcp_f32_e32 v37, v37
	v_rcp_f32_e32 v38, v38
	v_rcp_f32_e32 v39, v39
	v_pk_fma_f32 v[44:45], v[152:153], v[40:41], v[44:45]
	v_pk_fma_f32 v[46:47], v[154:155], v[42:43], v[46:47]
	v_lshl_add_u64 v[40:41], v[176:177], 0, s[22:23]
	v_pk_mul_f32 v[36:37], v[36:37], v[44:45]
	v_pk_mul_f32 v[38:39], v[38:39], v[46:47]
	global_store_dwordx4 v[40:41], v[36:39], off nt
	s_nop 1
	v_pk_mul_f32 v[36:37], v[36:37], s[96:97] op_sel_hi:[1,0]
	v_pk_mul_f32 v[38:39], v[38:39], s[96:97] op_sel_hi:[1,0]
	v_exp_f32_e32 v32, v32
	v_exp_f32_e32 v33, v33
	v_exp_f32_e32 v34, v34
	v_pk_fma_f32 v[32:33], v[32:33], s[98:99], s[98:99] op_sel_hi:[1,0,0]
	v_exp_f32_e32 v35, v35
	v_exp_f32_e32 v36, v36
	v_pk_fma_f32 v[34:35], v[34:35], s[98:99], s[98:99] op_sel_hi:[1,0,0]
	v_exp_f32_e32 v37, v37
	v_exp_f32_e32 v38, v38
	v_pk_add_f32 v[36:37], v[36:37], 1.0 op_sel_hi:[1,0]
	v_exp_f32_e32 v39, v39
	v_pk_mul_f32 v[32:33], v[32:33], v[36:37]
	v_rcp_f32_e32 v32, v32
	v_pk_add_f32 v[38:39], v[38:39], 1.0 op_sel_hi:[1,0]
	v_rcp_f32_e32 v33, v33
	v_pk_mul_f32 v[34:35], v[34:35], v[38:39]
	v_pk_add_f32 v[36:37], v[36:37], 2.0 op_sel_hi:[1,0] neg_lo:[1,0] neg_hi:[1,0]
	v_rcp_f32_e32 v34, v34
	v_rcp_f32_e32 v35, v35
	v_pk_add_f32 v[38:39], v[38:39], 2.0 op_sel_hi:[1,0] neg_lo:[1,0] neg_hi:[1,0]
	v_pk_mul_f32 v[32:33], v[32:33], v[36:37]
	v_pk_mul_f32 v[34:35], v[34:35], v[38:39]
	v_cvt_pk_fp8_f32 v40, v32, v33
	v_or_b32_e32 v36, 16, v200
	v_ashrrev_i32_e32 v37, 31, v36
	v_lshlrev_b64 v[36:37], 10, v[36:37]
	v_cvt_pk_fp8_f32 v40, v34, v35 op_sel:[0,0,1]
	v_lshl_add_u64 v[38:39], v[122:123], 0, v[36:37]
	global_store_dword v[38:39], v40, off
	v_pk_mul_f32 v[32:33], v[32:33], s[98:99] op_sel_hi:[1,0]
	v_pk_mul_f32 v[34:35], v[34:35], s[98:99] op_sel_hi:[1,0]
	v_cvt_pk_f16_f32 v32, v32, v33
	v_cvt_pk_f16_f32 v33, v34, v35
	v_lshl_add_u64 v[34:35], v[36:37], 1, v[120:121]
	global_store_dwordx2 v[34:35], v[32:33], off
	v_exp_f32_e32 v24, v24
	v_exp_f32_e32 v25, v25
	v_exp_f32_e32 v26, v26
	v_pk_add_f32 v[24:25], v[24:25], 1.0 op_sel_hi:[1,0]
	v_exp_f32_e32 v27, v27
	v_exp_f32_e32 v28, v28
	v_pk_add_f32 v[26:27], v[26:27], 1.0 op_sel_hi:[1,0]
	v_exp_f32_e32 v29, v29
	v_exp_f32_e32 v30, v30
	v_pk_add_f32 v[28:29], v[28:29], 1.0 op_sel_hi:[1,0]
	v_exp_f32_e32 v31, v31
	v_exp_f32_e32 v20, v20
	v_pk_add_f32 v[30:31], v[30:31], 1.0 op_sel_hi:[1,0]
	v_exp_f32_e32 v21, v21
	v_pk_mul_f32 v[24:25], v[24:25], v[28:29]
	v_exp_f32_e32 v22, v22
	v_pk_mul_f32 v[26:27], v[26:27], v[30:31]
	v_exp_f32_e32 v23, v23
	v_pk_add_f32 v[28:29], v[28:29], 2.0 op_sel_hi:[1,0] neg_lo:[1,0] neg_hi:[1,0]
	v_pk_add_f32 v[20:21], v[20:21], 1.0 op_sel_hi:[1,0]
	v_pk_add_f32 v[30:31], v[30:31], 2.0 op_sel_hi:[1,0] neg_lo:[1,0] neg_hi:[1,0]
	v_pk_add_f32 v[22:23], v[22:23], 1.0 op_sel_hi:[1,0]
	v_pk_mul_f32 v[28:29], v[28:29], v[20:21]
	v_pk_mul_f32 v[20:21], v[20:21], v[24:25]
	v_pk_mul_f32 v[30:31], v[30:31], v[22:23]
	v_pk_mul_f32 v[22:23], v[22:23], v[26:27]
	v_rcp_f32_e32 v20, v20
	v_rcp_f32_e32 v21, v21
	v_rcp_f32_e32 v22, v22
	v_rcp_f32_e32 v23, v23
	v_pk_fma_f32 v[28:29], v[148:149], v[24:25], v[28:29]
	v_pk_fma_f32 v[30:31], v[150:151], v[26:27], v[30:31]
	v_pk_mul_f32 v[20:21], v[20:21], v[28:29]
	v_pk_mul_f32 v[22:23], v[22:23], v[30:31]
	v_lshl_add_u64 v[24:25], v[176:177], 0, s[16:17]
	global_store_dwordx4 v[24:25], v[20:23], off nt
	s_nop 1
	v_pk_mul_f32 v[20:21], v[20:21], s[96:97] op_sel_hi:[1,0]
	v_pk_mul_f32 v[22:23], v[22:23], s[96:97] op_sel_hi:[1,0]
	v_exp_f32_e32 v16, v16
	v_exp_f32_e32 v17, v17
	v_exp_f32_e32 v18, v18
	v_pk_fma_f32 v[16:17], v[16:17], s[98:99], s[98:99] op_sel_hi:[1,0,0]
	v_exp_f32_e32 v19, v19
	v_exp_f32_e32 v20, v20
	v_pk_fma_f32 v[18:19], v[18:19], s[98:99], s[98:99] op_sel_hi:[1,0,0]
	v_exp_f32_e32 v21, v21
	v_exp_f32_e32 v22, v22
	v_pk_add_f32 v[20:21], v[20:21], 1.0 op_sel_hi:[1,0]
	v_exp_f32_e32 v23, v23
	v_pk_mul_f32 v[16:17], v[16:17], v[20:21]
	v_rcp_f32_e32 v16, v16
	v_pk_add_f32 v[22:23], v[22:23], 1.0 op_sel_hi:[1,0]
	v_rcp_f32_e32 v17, v17
	v_pk_mul_f32 v[18:19], v[18:19], v[22:23]
	v_pk_add_f32 v[20:21], v[20:21], 2.0 op_sel_hi:[1,0] neg_lo:[1,0] neg_hi:[1,0]
	v_rcp_f32_e32 v18, v18
	v_rcp_f32_e32 v19, v19
	v_pk_add_f32 v[22:23], v[22:23], 2.0 op_sel_hi:[1,0] neg_lo:[1,0] neg_hi:[1,0]
	v_pk_mul_f32 v[16:17], v[16:17], v[20:21]
	v_pk_mul_f32 v[18:19], v[18:19], v[22:23]
	v_cvt_pk_fp8_f32 v24, v16, v17
	v_or_b32_e32 v20, 32, v200
	v_ashrrev_i32_e32 v21, 31, v20
	v_lshlrev_b64 v[20:21], 10, v[20:21]
	v_cvt_pk_fp8_f32 v24, v18, v19 op_sel:[0,0,1]
	v_lshl_add_u64 v[22:23], v[122:123], 0, v[20:21]
	global_store_dword v[22:23], v24, off
	v_pk_mul_f32 v[16:17], v[16:17], s[98:99] op_sel_hi:[1,0]
	v_pk_mul_f32 v[18:19], v[18:19], s[98:99] op_sel_hi:[1,0]
	v_cvt_pk_f16_f32 v16, v16, v17
	v_cvt_pk_f16_f32 v17, v18, v19
	v_lshl_add_u64 v[18:19], v[20:21], 1, v[120:121]
	global_store_dwordx2 v[18:19], v[16:17], off
	v_exp_f32_e32 v8, v8
	v_exp_f32_e32 v9, v9
	v_exp_f32_e32 v10, v10
	v_pk_add_f32 v[8:9], v[8:9], 1.0 op_sel_hi:[1,0]
	v_exp_f32_e32 v11, v11
	v_exp_f32_e32 v12, v12
	v_pk_add_f32 v[10:11], v[10:11], 1.0 op_sel_hi:[1,0]
	v_exp_f32_e32 v13, v13
	v_exp_f32_e32 v14, v14
	v_pk_add_f32 v[12:13], v[12:13], 1.0 op_sel_hi:[1,0]
	v_exp_f32_e32 v15, v15
	v_exp_f32_e32 v4, v4
	v_pk_add_f32 v[14:15], v[14:15], 1.0 op_sel_hi:[1,0]
	v_exp_f32_e32 v5, v5
	v_pk_mul_f32 v[8:9], v[8:9], v[12:13]
	v_exp_f32_e32 v6, v6
	v_pk_mul_f32 v[10:11], v[10:11], v[14:15]
	v_exp_f32_e32 v7, v7
	v_pk_add_f32 v[12:13], v[12:13], 2.0 op_sel_hi:[1,0] neg_lo:[1,0] neg_hi:[1,0]
	v_pk_add_f32 v[4:5], v[4:5], 1.0 op_sel_hi:[1,0]
	v_pk_add_f32 v[14:15], v[14:15], 2.0 op_sel_hi:[1,0] neg_lo:[1,0] neg_hi:[1,0]
	v_pk_add_f32 v[6:7], v[6:7], 1.0 op_sel_hi:[1,0]
	v_pk_mul_f32 v[12:13], v[12:13], v[4:5]
	v_pk_mul_f32 v[4:5], v[4:5], v[8:9]
	v_pk_mul_f32 v[14:15], v[14:15], v[6:7]
	v_pk_mul_f32 v[6:7], v[6:7], v[10:11]
	v_rcp_f32_e32 v4, v4
	v_rcp_f32_e32 v5, v5
	v_rcp_f32_e32 v6, v6
	v_rcp_f32_e32 v7, v7
	v_pk_fma_f32 v[12:13], v[144:145], v[8:9], v[12:13]
	v_pk_fma_f32 v[14:15], v[146:147], v[10:11], v[14:15]
	v_lshl_add_u64 v[8:9], v[176:177], 0, s[24:25]
	v_pk_mul_f32 v[4:5], v[4:5], v[12:13]
	v_pk_mul_f32 v[6:7], v[6:7], v[14:15]
	global_store_dwordx4 v[8:9], v[4:7], off nt
	s_nop 1
	v_pk_mul_f32 v[4:5], v[4:5], s[96:97] op_sel_hi:[1,0]
	v_pk_mul_f32 v[6:7], v[6:7], s[96:97] op_sel_hi:[1,0]
	v_exp_f32_e32 v0, v0
	v_exp_f32_e32 v1, v1
	v_exp_f32_e32 v2, v2
	v_pk_fma_f32 v[0:1], v[0:1], s[98:99], s[98:99] op_sel_hi:[1,0,0]
	v_exp_f32_e32 v3, v3
	v_exp_f32_e32 v4, v4
	v_pk_fma_f32 v[2:3], v[2:3], s[98:99], s[98:99] op_sel_hi:[1,0,0]
	v_exp_f32_e32 v5, v5
	v_exp_f32_e32 v6, v6
	v_pk_add_f32 v[4:5], v[4:5], 1.0 op_sel_hi:[1,0]
	v_exp_f32_e32 v7, v7
	v_pk_mul_f32 v[0:1], v[0:1], v[4:5]
	v_rcp_f32_e32 v0, v0
	v_pk_add_f32 v[6:7], v[6:7], 1.0 op_sel_hi:[1,0]
	v_rcp_f32_e32 v1, v1
	v_pk_mul_f32 v[2:3], v[2:3], v[6:7]
	v_pk_add_f32 v[4:5], v[4:5], 2.0 op_sel_hi:[1,0] neg_lo:[1,0] neg_hi:[1,0]
	v_rcp_f32_e32 v2, v2
	v_rcp_f32_e32 v3, v3
	v_pk_add_f32 v[6:7], v[6:7], 2.0 op_sel_hi:[1,0] neg_lo:[1,0] neg_hi:[1,0]
	v_pk_mul_f32 v[0:1], v[0:1], v[4:5]
	v_pk_mul_f32 v[2:3], v[2:3], v[6:7]
	v_cvt_pk_fp8_f32 v8, v0, v1
	v_or_b32_e32 v4, 48, v200
	v_ashrrev_i32_e32 v5, 31, v4
	v_lshlrev_b64 v[4:5], 10, v[4:5]
	v_cvt_pk_fp8_f32 v8, v2, v3 op_sel:[0,0,1]
	v_lshl_add_u64 v[6:7], v[122:123], 0, v[4:5]
	global_store_dword v[6:7], v8, off
	v_pk_mul_f32 v[0:1], v[0:1], s[98:99] op_sel_hi:[1,0]
	v_pk_mul_f32 v[2:3], v[2:3], s[98:99] op_sel_hi:[1,0]
	v_cvt_pk_f16_f32 v0, v0, v1
	v_cvt_pk_f16_f32 v1, v2, v3
	v_lshl_add_u64 v[2:3], v[4:5], 1, v[120:121]
	global_store_dwordx2 v[2:3], v[0:1], off
	s_branch .LBB2_24
.Lmy_epi_last:
	s_cmp_eq_u32 s30, 7
	s_cbranch_scc1 .Lmy_epi_l7
	v_exp_f32_e32 v120, v120
	v_exp_f32_e32 v121, v121
	v_exp_f32_e32 v122, v122
	v_pk_add_f32 v[120:121], v[120:121], 1.0 op_sel_hi:[1,0]
	v_exp_f32_e32 v123, v123
	v_exp_f32_e32 v124, v124
	v_pk_add_f32 v[122:123], v[122:123], 1.0 op_sel_hi:[1,0]
	v_exp_f32_e32 v125, v125
	v_exp_f32_e32 v126, v126
	v_pk_add_f32 v[124:125], v[124:125], 1.0 op_sel_hi:[1,0]
	v_exp_f32_e32 v127, v127
	v_exp_f32_e32 v116, v116
	v_pk_add_f32 v[126:127], v[126:127], 1.0 op_sel_hi:[1,0]
	v_exp_f32_e32 v117, v117
	v_pk_mul_f32 v[120:121], v[120:121], v[124:125]
	v_exp_f32_e32 v118, v118
	v_pk_mul_f32 v[122:123], v[122:123], v[126:127]
	v_exp_f32_e32 v119, v119
	v_pk_add_f32 v[124:125], v[124:125], 2.0 op_sel_hi:[1,0] neg_lo:[1,0] neg_hi:[1,0]
	v_pk_add_f32 v[116:117], v[116:117], 1.0 op_sel_hi:[1,0]
	v_pk_add_f32 v[126:127], v[126:127], 2.0 op_sel_hi:[1,0] neg_lo:[1,0] neg_hi:[1,0]
	v_pk_add_f32 v[118:119], v[118:119], 1.0 op_sel_hi:[1,0]
	v_pk_mul_f32 v[124:125], v[124:125], v[116:117]
	v_pk_mul_f32 v[116:117], v[116:117], v[120:121]
	v_pk_mul_f32 v[126:127], v[126:127], v[118:119]
	v_pk_mul_f32 v[118:119], v[118:119], v[122:123]
	v_rcp_f32_e32 v116, v116
	v_rcp_f32_e32 v117, v117
	v_rcp_f32_e32 v118, v118
	v_rcp_f32_e32 v119, v119
	s_waitcnt lgkmcnt(3)
	v_pk_fma_f32 v[124:125], v[172:173], v[120:121], v[124:125]
	v_pk_fma_f32 v[126:127], v[174:175], v[122:123], v[126:127]
	v_pk_mul_f32 v[116:117], v[116:117], v[124:125]
	v_pk_mul_f32 v[118:119], v[118:119], v[126:127]
	global_store_dwordx4 v[176:177], v[116:119], off sc1
	s_nop 1
	v_pk_mul_f32 v[116:117], v[116:117], s[96:97] op_sel_hi:[1,0]
	v_pk_mul_f32 v[118:119], v[118:119], s[96:97] op_sel_hi:[1,0]
	v_exp_f32_e32 v112, v112
	v_exp_f32_e32 v113, v113
	v_exp_f32_e32 v114, v114
	v_pk_fma_f32 v[112:113], v[112:113], s[98:99], s[98:99] op_sel_hi:[1,0,0]
	v_exp_f32_e32 v115, v115
	v_exp_f32_e32 v116, v116
	v_pk_fma_f32 v[114:115], v[114:115], s[98:99], s[98:99] op_sel_hi:[1,0,0]
	v_exp_f32_e32 v117, v117
	v_exp_f32_e32 v118, v118
	v_pk_add_f32 v[116:117], v[116:117], 1.0 op_sel_hi:[1,0]
	v_exp_f32_e32 v119, v119
	v_pk_mul_f32 v[112:113], v[112:113], v[116:117]
	v_rcp_f32_e32 v112, v112
	v_pk_add_f32 v[118:119], v[118:119], 1.0 op_sel_hi:[1,0]
	v_rcp_f32_e32 v113, v113
	v_pk_mul_f32 v[114:115], v[114:115], v[118:119]
	v_pk_add_f32 v[116:117], v[116:117], 2.0 op_sel_hi:[1,0] neg_lo:[1,0] neg_hi:[1,0]
	v_rcp_f32_e32 v114, v114
	v_rcp_f32_e32 v115, v115
	v_pk_add_f32 v[118:119], v[118:119], 2.0 op_sel_hi:[1,0] neg_lo:[1,0] neg_hi:[1,0]
	v_pk_mul_f32 v[112:113], v[112:113], v[116:117]
	v_pk_mul_f32 v[114:115], v[114:115], v[118:119]
	v_cvt_pk_fp8_f32 v124, v112, v113
	s_add_u32 s0, s8, s27
	s_addc_u32 s1, s9, 0
	s_ashr_i32 s35, s34, 31
	s_lshl_b64 s[34:35], s[34:35], 21
	v_ashrrev_i32_e32 v209, 31, v208
	s_add_u32 s36, s73, s34
	v_lshl_add_u64 v[122:123], s[0:1], 0, v[210:211]
	v_cvt_pk_fp8_f32 v124, v114, v115 op_sel:[0,0,1]
	v_lshlrev_b64 v[116:117], 10, v[208:209]
	s_addc_u32 s37, s74, s35
	v_lshl_add_u64 v[118:119], v[122:123], 0, v[116:117]
	global_store_dword v[118:119], v124, off
	s_cmp_eq_u32 s30, 7
	s_cselect_b64 s[34:35], -1, 0
	s_cmp_lg_u32 s30, 7
	v_lshl_add_u64 v[120:121], v[210:211], 1, s[36:37]
	v_exp_f32_e32 v104, v104
	v_exp_f32_e32 v105, v105
	v_exp_f32_e32 v106, v106
	v_pk_add_f32 v[104:105], v[104:105], 1.0 op_sel_hi:[1,0]
	v_exp_f32_e32 v107, v107
	v_exp_f32_e32 v108, v108
	v_pk_add_f32 v[106:107], v[106:107], 1.0 op_sel_hi:[1,0]
	v_exp_f32_e32 v109, v109
	v_exp_f32_e32 v110, v110
	v_pk_add_f32 v[108:109], v[108:109], 1.0 op_sel_hi:[1,0]
	v_exp_f32_e32 v111, v111
	v_exp_f32_e32 v100, v100
	v_pk_add_f32 v[110:111], v[110:111], 1.0 op_sel_hi:[1,0]
	v_exp_f32_e32 v101, v101
	v_pk_mul_f32 v[104:105], v[104:105], v[108:109]
	v_exp_f32_e32 v102, v102
	v_pk_mul_f32 v[106:107], v[106:107], v[110:111]
	v_exp_f32_e32 v103, v103
	v_pk_add_f32 v[108:109], v[108:109], 2.0 op_sel_hi:[1,0] neg_lo:[1,0] neg_hi:[1,0]
	v_pk_add_f32 v[100:101], v[100:101], 1.0 op_sel_hi:[1,0]
	v_pk_add_f32 v[110:111], v[110:111], 2.0 op_sel_hi:[1,0] neg_lo:[1,0] neg_hi:[1,0]
	v_pk_add_f32 v[102:103], v[102:103], 1.0 op_sel_hi:[1,0]
	v_pk_mul_f32 v[108:109], v[108:109], v[100:101]
	v_pk_mul_f32 v[100:101], v[100:101], v[104:105]
	v_pk_mul_f32 v[110:111], v[110:111], v[102:103]
	v_pk_mul_f32 v[102:103], v[102:103], v[106:107]
	v_rcp_f32_e32 v100, v100
	v_rcp_f32_e32 v101, v101
	v_rcp_f32_e32 v102, v102
	v_rcp_f32_e32 v103, v103
	s_waitcnt lgkmcnt(2)
	v_pk_fma_f32 v[108:109], v[168:169], v[104:105], v[108:109]
	v_pk_fma_f32 v[110:111], v[170:171], v[106:107], v[110:111]
	v_lshl_add_u64 v[104:105], v[176:177], 0, s[18:19]
	v_pk_mul_f32 v[100:101], v[100:101], v[108:109]
	v_pk_mul_f32 v[102:103], v[102:103], v[110:111]
	global_store_dwordx4 v[104:105], v[100:103], off sc1
	s_nop 1
	v_pk_mul_f32 v[100:101], v[100:101], s[96:97] op_sel_hi:[1,0]
	v_pk_mul_f32 v[102:103], v[102:103], s[96:97] op_sel_hi:[1,0]
	v_exp_f32_e32 v96, v96
	v_exp_f32_e32 v97, v97
	v_exp_f32_e32 v98, v98
	v_pk_fma_f32 v[96:97], v[96:97], s[98:99], s[98:99] op_sel_hi:[1,0,0]
	v_exp_f32_e32 v99, v99
	v_exp_f32_e32 v100, v100
	v_pk_fma_f32 v[98:99], v[98:99], s[98:99], s[98:99] op_sel_hi:[1,0,0]
	v_exp_f32_e32 v101, v101
	v_exp_f32_e32 v102, v102
	v_pk_add_f32 v[100:101], v[100:101], 1.0 op_sel_hi:[1,0]
	v_exp_f32_e32 v103, v103
	v_pk_mul_f32 v[96:97], v[96:97], v[100:101]
	v_rcp_f32_e32 v96, v96
	v_pk_add_f32 v[102:103], v[102:103], 1.0 op_sel_hi:[1,0]
	v_rcp_f32_e32 v97, v97
	v_pk_mul_f32 v[98:99], v[98:99], v[102:103]
	v_pk_add_f32 v[100:101], v[100:101], 2.0 op_sel_hi:[1,0] neg_lo:[1,0] neg_hi:[1,0]
	v_rcp_f32_e32 v98, v98
	v_rcp_f32_e32 v99, v99
	v_pk_add_f32 v[102:103], v[102:103], 2.0 op_sel_hi:[1,0] neg_lo:[1,0] neg_hi:[1,0]
	v_pk_mul_f32 v[96:97], v[96:97], v[100:101]
	v_pk_mul_f32 v[98:99], v[98:99], v[102:103]
	v_cvt_pk_fp8_f32 v104, v96, v97
	v_ashrrev_i32_e32 v207, 31, v206
	v_lshlrev_b64 v[100:101], 10, v[206:207]
	v_lshl_add_u64 v[102:103], v[122:123], 0, v[100:101]
	v_cvt_pk_fp8_f32 v104, v98, v99 op_sel:[0,0,1]
	v_cndmask_b32_e64 v105, 0, 1, s[34:35]
	global_store_dword v[102:103], v104, off
	v_cmp_ne_u32_e64 s[0:1], 1, v105
	v_exp_f32_e32 v88, v88
	v_exp_f32_e32 v89, v89
	v_exp_f32_e32 v90, v90
	v_pk_add_f32 v[88:89], v[88:89], 1.0 op_sel_hi:[1,0]
	v_exp_f32_e32 v91, v91
	v_exp_f32_e32 v92, v92
	v_pk_add_f32 v[90:91], v[90:91], 1.0 op_sel_hi:[1,0]
	v_exp_f32_e32 v93, v93
	v_exp_f32_e32 v94, v94
	v_pk_add_f32 v[92:93], v[92:93], 1.0 op_sel_hi:[1,0]
	v_exp_f32_e32 v95, v95
	v_exp_f32_e32 v84, v84
	v_pk_add_f32 v[94:95], v[94:95], 1.0 op_sel_hi:[1,0]
	v_exp_f32_e32 v85, v85
	v_pk_mul_f32 v[88:89], v[88:89], v[92:93]
	v_exp_f32_e32 v86, v86
	v_pk_mul_f32 v[90:91], v[90:91], v[94:95]
	v_exp_f32_e32 v87, v87
	v_pk_add_f32 v[92:93], v[92:93], 2.0 op_sel_hi:[1,0] neg_lo:[1,0] neg_hi:[1,0]
	v_pk_add_f32 v[84:85], v[84:85], 1.0 op_sel_hi:[1,0]
	v_pk_add_f32 v[94:95], v[94:95], 2.0 op_sel_hi:[1,0] neg_lo:[1,0] neg_hi:[1,0]
	v_pk_add_f32 v[86:87], v[86:87], 1.0 op_sel_hi:[1,0]
	v_pk_mul_f32 v[92:93], v[92:93], v[84:85]
	v_pk_mul_f32 v[84:85], v[84:85], v[88:89]
	v_pk_mul_f32 v[94:95], v[94:95], v[86:87]
	v_pk_mul_f32 v[86:87], v[86:87], v[90:91]
	v_rcp_f32_e32 v84, v84
	v_rcp_f32_e32 v85, v85
	v_rcp_f32_e32 v86, v86
	v_rcp_f32_e32 v87, v87
	s_waitcnt lgkmcnt(1)
	v_pk_fma_f32 v[92:93], v[164:165], v[88:89], v[92:93]
	v_pk_fma_f32 v[94:95], v[166:167], v[90:91], v[94:95]
	v_pk_mul_f32 v[84:85], v[84:85], v[92:93]
	v_pk_mul_f32 v[86:87], v[86:87], v[94:95]
	v_lshl_add_u64 v[88:89], v[176:177], 0, s[12:13]
	global_store_dwordx4 v[88:89], v[84:87], off sc1
	s_nop 1
	v_pk_mul_f32 v[84:85], v[84:85], s[96:97] op_sel_hi:[1,0]
	v_pk_mul_f32 v[86:87], v[86:87], s[96:97] op_sel_hi:[1,0]
	v_exp_f32_e32 v80, v80
	v_exp_f32_e32 v81, v81
	v_exp_f32_e32 v82, v82
	v_pk_fma_f32 v[80:81], v[80:81], s[98:99], s[98:99] op_sel_hi:[1,0,0]
	v_exp_f32_e32 v83, v83
	v_exp_f32_e32 v84, v84
	v_pk_fma_f32 v[82:83], v[82:83], s[98:99], s[98:99] op_sel_hi:[1,0,0]
	v_exp_f32_e32 v85, v85
	v_exp_f32_e32 v86, v86
	v_pk_add_f32 v[84:85], v[84:85], 1.0 op_sel_hi:[1,0]
	v_exp_f32_e32 v87, v87
	v_pk_mul_f32 v[80:81], v[80:81], v[84:85]
	v_rcp_f32_e32 v80, v80
	v_pk_add_f32 v[86:87], v[86:87], 1.0 op_sel_hi:[1,0]
	v_rcp_f32_e32 v81, v81
	v_pk_mul_f32 v[82:83], v[82:83], v[86:87]
	v_pk_add_f32 v[84:85], v[84:85], 2.0 op_sel_hi:[1,0] neg_lo:[1,0] neg_hi:[1,0]
	v_rcp_f32_e32 v82, v82
	v_rcp_f32_e32 v83, v83
	v_pk_add_f32 v[86:87], v[86:87], 2.0 op_sel_hi:[1,0] neg_lo:[1,0] neg_hi:[1,0]
	v_pk_mul_f32 v[80:81], v[80:81], v[84:85]
	v_pk_mul_f32 v[82:83], v[82:83], v[86:87]
	v_ashrrev_i32_e32 v205, 31, v204
	v_cvt_pk_fp8_f32 v88, v80, v81
	s_and_b64 vcc, exec, s[0:1]
	v_cvt_pk_fp8_f32 v88, v82, v83 op_sel:[0,0,1]
	v_lshlrev_b64 v[84:85], 10, v[204:205]
	v_lshl_add_u64 v[86:87], v[122:123], 0, v[84:85]
	global_store_dword v[86:87], v88, off
	v_exp_f32_e32 v72, v72
	v_exp_f32_e32 v73, v73
	v_exp_f32_e32 v74, v74
	v_pk_add_f32 v[72:73], v[72:73], 1.0 op_sel_hi:[1,0]
	v_exp_f32_e32 v75, v75
	v_exp_f32_e32 v76, v76
	v_pk_add_f32 v[74:75], v[74:75], 1.0 op_sel_hi:[1,0]
	v_exp_f32_e32 v77, v77
	v_exp_f32_e32 v78, v78
	v_pk_add_f32 v[76:77], v[76:77], 1.0 op_sel_hi:[1,0]
	v_exp_f32_e32 v79, v79
	v_exp_f32_e32 v68, v68
	v_pk_add_f32 v[78:79], v[78:79], 1.0 op_sel_hi:[1,0]
	v_exp_f32_e32 v69, v69
	v_pk_mul_f32 v[72:73], v[72:73], v[76:77]
	v_exp_f32_e32 v70, v70
	v_pk_mul_f32 v[74:75], v[74:75], v[78:79]
	v_exp_f32_e32 v71, v71
	v_pk_add_f32 v[76:77], v[76:77], 2.0 op_sel_hi:[1,0] neg_lo:[1,0] neg_hi:[1,0]
	v_pk_add_f32 v[68:69], v[68:69], 1.0 op_sel_hi:[1,0]
	v_pk_add_f32 v[78:79], v[78:79], 2.0 op_sel_hi:[1,0] neg_lo:[1,0] neg_hi:[1,0]
	v_pk_add_f32 v[70:71], v[70:71], 1.0 op_sel_hi:[1,0]
	v_pk_mul_f32 v[76:77], v[76:77], v[68:69]
	v_pk_mul_f32 v[68:69], v[68:69], v[72:73]
	v_pk_mul_f32 v[78:79], v[78:79], v[70:71]
	v_pk_mul_f32 v[70:71], v[70:71], v[74:75]
	v_rcp_f32_e32 v68, v68
	v_rcp_f32_e32 v69, v69
	v_rcp_f32_e32 v70, v70
	v_rcp_f32_e32 v71, v71
	s_waitcnt lgkmcnt(0)
	v_pk_fma_f32 v[76:77], v[160:161], v[72:73], v[76:77]
	v_pk_fma_f32 v[78:79], v[162:163], v[74:75], v[78:79]
	v_lshl_add_u64 v[72:73], v[176:177], 0, s[20:21]
	v_pk_mul_f32 v[68:69], v[68:69], v[76:77]
	v_pk_mul_f32 v[70:71], v[70:71], v[78:79]
	global_store_dwordx4 v[72:73], v[68:71], off sc1
	s_nop 1
	v_pk_mul_f32 v[68:69], v[68:69], s[96:97] op_sel_hi:[1,0]
	v_pk_mul_f32 v[70:71], v[70:71], s[96:97] op_sel_hi:[1,0]
	v_exp_f32_e32 v64, v64
	v_exp_f32_e32 v65, v65
	v_exp_f32_e32 v66, v66
	v_pk_fma_f32 v[64:65], v[64:65], s[98:99], s[98:99] op_sel_hi:[1,0,0]
	v_exp_f32_e32 v67, v67
	v_exp_f32_e32 v68, v68
	v_pk_fma_f32 v[66:67], v[66:67], s[98:99], s[98:99] op_sel_hi:[1,0,0]
	v_exp_f32_e32 v69, v69
	v_exp_f32_e32 v70, v70
	v_pk_add_f32 v[68:69], v[68:69], 1.0 op_sel_hi:[1,0]
	v_exp_f32_e32 v71, v71
	v_pk_mul_f32 v[64:65], v[64:65], v[68:69]
	v_rcp_f32_e32 v64, v64
	v_pk_add_f32 v[70:71], v[70:71], 1.0 op_sel_hi:[1,0]
	v_rcp_f32_e32 v65, v65
	v_pk_mul_f32 v[66:67], v[66:67], v[70:71]
	v_pk_add_f32 v[68:69], v[68:69], 2.0 op_sel_hi:[1,0] neg_lo:[1,0] neg_hi:[1,0]
	v_rcp_f32_e32 v66, v66
	v_rcp_f32_e32 v67, v67
	v_pk_add_f32 v[70:71], v[70:71], 2.0 op_sel_hi:[1,0] neg_lo:[1,0] neg_hi:[1,0]
	v_pk_mul_f32 v[64:65], v[64:65], v[68:69]
	v_pk_mul_f32 v[66:67], v[66:67], v[70:71]
	v_ashrrev_i32_e32 v203, 31, v202
	v_cvt_pk_fp8_f32 v72, v64, v65
	s_and_b64 vcc, exec, s[0:1]
	v_cvt_pk_fp8_f32 v72, v66, v67 op_sel:[0,0,1]
	v_lshlrev_b64 v[68:69], 10, v[202:203]
	v_lshl_add_u64 v[70:71], v[122:123], 0, v[68:69]
	global_store_dword v[70:71], v72, off
	v_exp_f32_e32 v56, v56
	v_exp_f32_e32 v57, v57
	v_exp_f32_e32 v58, v58
	v_pk_add_f32 v[56:57], v[56:57], 1.0 op_sel_hi:[1,0]
	v_exp_f32_e32 v59, v59
	v_exp_f32_e32 v60, v60
	v_pk_add_f32 v[58:59], v[58:59], 1.0 op_sel_hi:[1,0]
	v_exp_f32_e32 v61, v61
	v_exp_f32_e32 v62, v62
	v_pk_add_f32 v[60:61], v[60:61], 1.0 op_sel_hi:[1,0]
	v_exp_f32_e32 v63, v63
	v_exp_f32_e32 v52, v52
	v_pk_add_f32 v[62:63], v[62:63], 1.0 op_sel_hi:[1,0]
	v_exp_f32_e32 v53, v53
	v_pk_mul_f32 v[56:57], v[56:57], v[60:61]
	v_exp_f32_e32 v54, v54
	v_pk_mul_f32 v[58:59], v[58:59], v[62:63]
	v_exp_f32_e32 v55, v55
	v_pk_add_f32 v[60:61], v[60:61], 2.0 op_sel_hi:[1,0] neg_lo:[1,0] neg_hi:[1,0]
	v_pk_add_f32 v[52:53], v[52:53], 1.0 op_sel_hi:[1,0]
	v_pk_add_f32 v[62:63], v[62:63], 2.0 op_sel_hi:[1,0] neg_lo:[1,0] neg_hi:[1,0]
	v_pk_add_f32 v[54:55], v[54:55], 1.0 op_sel_hi:[1,0]
	v_pk_mul_f32 v[60:61], v[60:61], v[52:53]
	v_pk_mul_f32 v[52:53], v[52:53], v[56:57]
	v_pk_mul_f32 v[62:63], v[62:63], v[54:55]
	v_pk_mul_f32 v[54:55], v[54:55], v[58:59]
	v_rcp_f32_e32 v52, v52
	v_rcp_f32_e32 v53, v53
	v_rcp_f32_e32 v54, v54
	v_rcp_f32_e32 v55, v55
	s_waitcnt vmcnt(8)
	v_pk_fma_f32 v[60:61], v[156:157], v[56:57], v[60:61]
	v_pk_fma_f32 v[62:63], v[158:159], v[58:59], v[62:63]
	v_pk_mul_f32 v[52:53], v[52:53], v[60:61]
	v_pk_mul_f32 v[54:55], v[54:55], v[62:63]
	v_lshl_add_u64 v[56:57], v[176:177], 0, s[14:15]
	global_store_dwordx4 v[56:57], v[52:55], off sc1
	s_nop 1
	v_pk_mul_f32 v[52:53], v[52:53], s[96:97] op_sel_hi:[1,0]
	v_pk_mul_f32 v[54:55], v[54:55], s[96:97] op_sel_hi:[1,0]
	v_exp_f32_e32 v48, v48
	v_exp_f32_e32 v49, v49
	v_exp_f32_e32 v50, v50
	v_pk_fma_f32 v[48:49], v[48:49], s[98:99], s[98:99] op_sel_hi:[1,0,0]
	v_exp_f32_e32 v51, v51
	v_exp_f32_e32 v52, v52
	v_pk_fma_f32 v[50:51], v[50:51], s[98:99], s[98:99] op_sel_hi:[1,0,0]
	v_exp_f32_e32 v53, v53
	v_exp_f32_e32 v54, v54
	v_pk_add_f32 v[52:53], v[52:53], 1.0 op_sel_hi:[1,0]
	v_exp_f32_e32 v55, v55
	v_pk_mul_f32 v[48:49], v[48:49], v[52:53]
	v_rcp_f32_e32 v48, v48
	v_pk_add_f32 v[54:55], v[54:55], 1.0 op_sel_hi:[1,0]
	v_rcp_f32_e32 v49, v49
	v_pk_mul_f32 v[50:51], v[50:51], v[54:55]
	v_pk_add_f32 v[52:53], v[52:53], 2.0 op_sel_hi:[1,0] neg_lo:[1,0] neg_hi:[1,0]
	v_rcp_f32_e32 v50, v50
	v_rcp_f32_e32 v51, v51
	v_pk_add_f32 v[54:55], v[54:55], 2.0 op_sel_hi:[1,0] neg_lo:[1,0] neg_hi:[1,0]
	v_pk_mul_f32 v[48:49], v[48:49], v[52:53]
	v_pk_mul_f32 v[50:51], v[50:51], v[54:55]
	v_ashrrev_i32_e32 v201, 31, v200
	v_cvt_pk_fp8_f32 v56, v48, v49
	s_and_b64 vcc, exec, s[0:1]
	v_cvt_pk_fp8_f32 v56, v50, v51 op_sel:[0,0,1]
	v_lshlrev_b64 v[52:53], 10, v[200:201]
	v_lshl_add_u64 v[54:55], v[122:123], 0, v[52:53]
	global_store_dword v[54:55], v56, off
	v_exp_f32_e32 v40, v40
	v_exp_f32_e32 v41, v41
	v_exp_f32_e32 v42, v42
	v_pk_add_f32 v[40:41], v[40:41], 1.0 op_sel_hi:[1,0]
	v_exp_f32_e32 v43, v43
	v_exp_f32_e32 v44, v44
	v_pk_add_f32 v[42:43], v[42:43], 1.0 op_sel_hi:[1,0]
	v_exp_f32_e32 v45, v45
	v_exp_f32_e32 v46, v46
	v_pk_add_f32 v[44:45], v[44:45], 1.0 op_sel_hi:[1,0]
	v_exp_f32_e32 v47, v47
	v_exp_f32_e32 v36, v36
	v_pk_add_f32 v[46:47], v[46:47], 1.0 op_sel_hi:[1,0]
	v_exp_f32_e32 v37, v37
	v_pk_mul_f32 v[40:41], v[40:41], v[44:45]
	v_exp_f32_e32 v38, v38
	v_pk_mul_f32 v[42:43], v[42:43], v[46:47]
	v_exp_f32_e32 v39, v39
	v_pk_add_f32 v[44:45], v[44:45], 2.0 op_sel_hi:[1,0] neg_lo:[1,0] neg_hi:[1,0]
	v_pk_add_f32 v[36:37], v[36:37], 1.0 op_sel_hi:[1,0]
	v_pk_add_f32 v[46:47], v[46:47], 2.0 op_sel_hi:[1,0] neg_lo:[1,0] neg_hi:[1,0]
	v_pk_add_f32 v[38:39], v[38:39], 1.0 op_sel_hi:[1,0]
	v_pk_mul_f32 v[44:45], v[44:45], v[36:37]
	v_pk_mul_f32 v[36:37], v[36:37], v[40:41]
	v_pk_mul_f32 v[46:47], v[46:47], v[38:39]
	v_pk_mul_f32 v[38:39], v[38:39], v[42:43]
	v_rcp_f32_e32 v36, v36
	v_rcp_f32_e32 v37, v37
	v_rcp_f32_e32 v38, v38
	v_rcp_f32_e32 v39, v39
	v_pk_fma_f32 v[44:45], v[152:153], v[40:41], v[44:45]
	v_pk_fma_f32 v[46:47], v[154:155], v[42:43], v[46:47]
	v_lshl_add_u64 v[40:41], v[176:177], 0, s[22:23]
	v_pk_mul_f32 v[36:37], v[36:37], v[44:45]
	v_pk_mul_f32 v[38:39], v[38:39], v[46:47]
	global_store_dwordx4 v[40:41], v[36:39], off sc1
	s_nop 1
	v_pk_mul_f32 v[36:37], v[36:37], s[96:97] op_sel_hi:[1,0]
	v_pk_mul_f32 v[38:39], v[38:39], s[96:97] op_sel_hi:[1,0]
	v_exp_f32_e32 v32, v32
	v_exp_f32_e32 v33, v33
	v_exp_f32_e32 v34, v34
	v_pk_fma_f32 v[32:33], v[32:33], s[98:99], s[98:99] op_sel_hi:[1,0,0]
	v_exp_f32_e32 v35, v35
	v_exp_f32_e32 v36, v36
	v_pk_fma_f32 v[34:35], v[34:35], s[98:99], s[98:99] op_sel_hi:[1,0,0]
	v_exp_f32_e32 v37, v37
	v_exp_f32_e32 v38, v38
	v_pk_add_f32 v[36:37], v[36:37], 1.0 op_sel_hi:[1,0]
	v_exp_f32_e32 v39, v39
	v_pk_mul_f32 v[32:33], v[32:33], v[36:37]
	v_rcp_f32_e32 v32, v32
	v_pk_add_f32 v[38:39], v[38:39], 1.0 op_sel_hi:[1,0]
	v_rcp_f32_e32 v33, v33
	v_pk_mul_f32 v[34:35], v[34:35], v[38:39]
	v_pk_add_f32 v[36:37], v[36:37], 2.0 op_sel_hi:[1,0] neg_lo:[1,0] neg_hi:[1,0]
	v_rcp_f32_e32 v34, v34
	v_rcp_f32_e32 v35, v35
	v_pk_add_f32 v[38:39], v[38:39], 2.0 op_sel_hi:[1,0] neg_lo:[1,0] neg_hi:[1,0]
	v_pk_mul_f32 v[32:33], v[32:33], v[36:37]
	v_pk_mul_f32 v[34:35], v[34:35], v[38:39]
	v_cvt_pk_fp8_f32 v40, v32, v33
	v_or_b32_e32 v36, 16, v200
	v_ashrrev_i32_e32 v37, 31, v36
	v_lshlrev_b64 v[36:37], 10, v[36:37]
	v_cvt_pk_fp8_f32 v40, v34, v35 op_sel:[0,0,1]
	v_lshl_add_u64 v[38:39], v[122:123], 0, v[36:37]
	global_store_dword v[38:39], v40, off
	v_exp_f32_e32 v24, v24
	v_exp_f32_e32 v25, v25
	v_exp_f32_e32 v26, v26
	v_pk_add_f32 v[24:25], v[24:25], 1.0 op_sel_hi:[1,0]
	v_exp_f32_e32 v27, v27
	v_exp_f32_e32 v28, v28
	v_pk_add_f32 v[26:27], v[26:27], 1.0 op_sel_hi:[1,0]
	v_exp_f32_e32 v29, v29
	v_exp_f32_e32 v30, v30
	v_pk_add_f32 v[28:29], v[28:29], 1.0 op_sel_hi:[1,0]
	v_exp_f32_e32 v31, v31
	v_exp_f32_e32 v20, v20
	v_pk_add_f32 v[30:31], v[30:31], 1.0 op_sel_hi:[1,0]
	v_exp_f32_e32 v21, v21
	v_pk_mul_f32 v[24:25], v[24:25], v[28:29]
	v_exp_f32_e32 v22, v22
	v_pk_mul_f32 v[26:27], v[26:27], v[30:31]
	v_exp_f32_e32 v23, v23
	v_pk_add_f32 v[28:29], v[28:29], 2.0 op_sel_hi:[1,0] neg_lo:[1,0] neg_hi:[1,0]
	v_pk_add_f32 v[20:21], v[20:21], 1.0 op_sel_hi:[1,0]
	v_pk_add_f32 v[30:31], v[30:31], 2.0 op_sel_hi:[1,0] neg_lo:[1,0] neg_hi:[1,0]
	v_pk_add_f32 v[22:23], v[22:23], 1.0 op_sel_hi:[1,0]
	v_pk_mul_f32 v[28:29], v[28:29], v[20:21]
	v_pk_mul_f32 v[20:21], v[20:21], v[24:25]
	v_pk_mul_f32 v[30:31], v[30:31], v[22:23]
	v_pk_mul_f32 v[22:23], v[22:23], v[26:27]
	v_rcp_f32_e32 v20, v20
	v_rcp_f32_e32 v21, v21
	v_rcp_f32_e32 v22, v22
	v_rcp_f32_e32 v23, v23
	v_pk_fma_f32 v[28:29], v[148:149], v[24:25], v[28:29]
	v_pk_fma_f32 v[30:31], v[150:151], v[26:27], v[30:31]
	v_pk_mul_f32 v[20:21], v[20:21], v[28:29]
	v_pk_mul_f32 v[22:23], v[22:23], v[30:31]
	v_lshl_add_u64 v[24:25], v[176:177], 0, s[16:17]
	global_store_dwordx4 v[24:25], v[20:23], off sc1
	s_nop 1
	v_pk_mul_f32 v[20:21], v[20:21], s[96:97] op_sel_hi:[1,0]
	v_pk_mul_f32 v[22:23], v[22:23], s[96:97] op_sel_hi:[1,0]
	v_exp_f32_e32 v16, v16
	v_exp_f32_e32 v17, v17
	v_exp_f32_e32 v18, v18
	v_pk_fma_f32 v[16:17], v[16:17], s[98:99], s[98:99] op_sel_hi:[1,0,0]
	v_exp_f32_e32 v19, v19
	v_exp_f32_e32 v20, v20
	v_pk_fma_f32 v[18:19], v[18:19], s[98:99], s[98:99] op_sel_hi:[1,0,0]
	v_exp_f32_e32 v21, v21
	v_exp_f32_e32 v22, v22
	v_pk_add_f32 v[20:21], v[20:21], 1.0 op_sel_hi:[1,0]
	v_exp_f32_e32 v23, v23
	v_pk_mul_f32 v[16:17], v[16:17], v[20:21]
	v_rcp_f32_e32 v16, v16
	v_pk_add_f32 v[22:23], v[22:23], 1.0 op_sel_hi:[1,0]
	v_rcp_f32_e32 v17, v17
	v_pk_mul_f32 v[18:19], v[18:19], v[22:23]
	v_pk_add_f32 v[20:21], v[20:21], 2.0 op_sel_hi:[1,0] neg_lo:[1,0] neg_hi:[1,0]
	v_rcp_f32_e32 v18, v18
	v_rcp_f32_e32 v19, v19
	v_pk_add_f32 v[22:23], v[22:23], 2.0 op_sel_hi:[1,0] neg_lo:[1,0] neg_hi:[1,0]
	v_pk_mul_f32 v[16:17], v[16:17], v[20:21]
	v_pk_mul_f32 v[18:19], v[18:19], v[22:23]
	v_cvt_pk_fp8_f32 v24, v16, v17
	v_or_b32_e32 v20, 32, v200
	v_ashrrev_i32_e32 v21, 31, v20
	v_lshlrev_b64 v[20:21], 10, v[20:21]
	v_cvt_pk_fp8_f32 v24, v18, v19 op_sel:[0,0,1]
	v_lshl_add_u64 v[22:23], v[122:123], 0, v[20:21]
	global_store_dword v[22:23], v24, off
	v_exp_f32_e32 v8, v8
	v_exp_f32_e32 v9, v9
	v_exp_f32_e32 v10, v10
	v_pk_add_f32 v[8:9], v[8:9], 1.0 op_sel_hi:[1,0]
	v_exp_f32_e32 v11, v11
	v_exp_f32_e32 v12, v12
	v_pk_add_f32 v[10:11], v[10:11], 1.0 op_sel_hi:[1,0]
	v_exp_f32_e32 v13, v13
	v_exp_f32_e32 v14, v14
	v_pk_add_f32 v[12:13], v[12:13], 1.0 op_sel_hi:[1,0]
	v_exp_f32_e32 v15, v15
	v_exp_f32_e32 v4, v4
	v_pk_add_f32 v[14:15], v[14:15], 1.0 op_sel_hi:[1,0]
	v_exp_f32_e32 v5, v5
	v_pk_mul_f32 v[8:9], v[8:9], v[12:13]
	v_exp_f32_e32 v6, v6
	v_pk_mul_f32 v[10:11], v[10:11], v[14:15]
	v_exp_f32_e32 v7, v7
	v_pk_add_f32 v[12:13], v[12:13], 2.0 op_sel_hi:[1,0] neg_lo:[1,0] neg_hi:[1,0]
	v_pk_add_f32 v[4:5], v[4:5], 1.0 op_sel_hi:[1,0]
	v_pk_add_f32 v[14:15], v[14:15], 2.0 op_sel_hi:[1,0] neg_lo:[1,0] neg_hi:[1,0]
	v_pk_add_f32 v[6:7], v[6:7], 1.0 op_sel_hi:[1,0]
	v_pk_mul_f32 v[12:13], v[12:13], v[4:5]
	v_pk_mul_f32 v[4:5], v[4:5], v[8:9]
	v_pk_mul_f32 v[14:15], v[14:15], v[6:7]
	v_pk_mul_f32 v[6:7], v[6:7], v[10:11]
	v_rcp_f32_e32 v4, v4
	v_rcp_f32_e32 v5, v5
	v_rcp_f32_e32 v6, v6
	v_rcp_f32_e32 v7, v7
	v_pk_fma_f32 v[12:13], v[144:145], v[8:9], v[12:13]
	v_pk_fma_f32 v[14:15], v[146:147], v[10:11], v[14:15]
	v_lshl_add_u64 v[8:9], v[176:177], 0, s[24:25]
	v_pk_mul_f32 v[4:5], v[4:5], v[12:13]
	v_pk_mul_f32 v[6:7], v[6:7], v[14:15]
	global_store_dwordx4 v[8:9], v[4:7], off sc1
	s_nop 1
	v_pk_mul_f32 v[4:5], v[4:5], s[96:97] op_sel_hi:[1,0]
	v_pk_mul_f32 v[6:7], v[6:7], s[96:97] op_sel_hi:[1,0]
	v_exp_f32_e32 v0, v0
	v_exp_f32_e32 v1, v1
	v_exp_f32_e32 v2, v2
	v_pk_fma_f32 v[0:1], v[0:1], s[98:99], s[98:99] op_sel_hi:[1,0,0]
	v_exp_f32_e32 v3, v3
	v_exp_f32_e32 v4, v4
	v_pk_fma_f32 v[2:3], v[2:3], s[98:99], s[98:99] op_sel_hi:[1,0,0]
	v_exp_f32_e32 v5, v5
	v_exp_f32_e32 v6, v6
	v_pk_add_f32 v[4:5], v[4:5], 1.0 op_sel_hi:[1,0]
	v_exp_f32_e32 v7, v7
	v_pk_mul_f32 v[0:1], v[0:1], v[4:5]
	v_rcp_f32_e32 v0, v0
	v_pk_add_f32 v[6:7], v[6:7], 1.0 op_sel_hi:[1,0]
	v_rcp_f32_e32 v1, v1
	v_pk_mul_f32 v[2:3], v[2:3], v[6:7]
	v_pk_add_f32 v[4:5], v[4:5], 2.0 op_sel_hi:[1,0] neg_lo:[1,0] neg_hi:[1,0]
	v_rcp_f32_e32 v2, v2
	v_rcp_f32_e32 v3, v3
	v_pk_add_f32 v[6:7], v[6:7], 2.0 op_sel_hi:[1,0] neg_lo:[1,0] neg_hi:[1,0]
	v_pk_mul_f32 v[0:1], v[0:1], v[4:5]
	v_pk_mul_f32 v[2:3], v[2:3], v[6:7]
	v_cvt_pk_fp8_f32 v8, v0, v1
	v_or_b32_e32 v4, 48, v200
	v_ashrrev_i32_e32 v5, 31, v4
	v_lshlrev_b64 v[4:5], 10, v[4:5]
	v_cvt_pk_fp8_f32 v8, v2, v3 op_sel:[0,0,1]
	v_lshl_add_u64 v[6:7], v[122:123], 0, v[4:5]
	global_store_dword v[6:7], v8, off
	s_branch .LBB2_24
.Lmy_epi_l7:
	v_exp_f32_e32 v120, v120
	v_exp_f32_e32 v121, v121
	v_exp_f32_e32 v122, v122
	v_pk_add_f32 v[120:121], v[120:121], 1.0 op_sel_hi:[1,0]
	v_exp_f32_e32 v123, v123
	v_exp_f32_e32 v124, v124
	v_pk_add_f32 v[122:123], v[122:123], 1.0 op_sel_hi:[1,0]
	v_exp_f32_e32 v125, v125
	v_exp_f32_e32 v126, v126
	v_pk_add_f32 v[124:125], v[124:125], 1.0 op_sel_hi:[1,0]
	v_exp_f32_e32 v127, v127
	v_exp_f32_e32 v116, v116
	v_pk_add_f32 v[126:127], v[126:127], 1.0 op_sel_hi:[1,0]
	v_exp_f32_e32 v117, v117
	v_pk_mul_f32 v[120:121], v[120:121], v[124:125]
	v_exp_f32_e32 v118, v118
	v_pk_mul_f32 v[122:123], v[122:123], v[126:127]
	v_exp_f32_e32 v119, v119
	v_pk_add_f32 v[124:125], v[124:125], 2.0 op_sel_hi:[1,0] neg_lo:[1,0] neg_hi:[1,0]
	v_pk_add_f32 v[116:117], v[116:117], 1.0 op_sel_hi:[1,0]
	v_pk_add_f32 v[126:127], v[126:127], 2.0 op_sel_hi:[1,0] neg_lo:[1,0] neg_hi:[1,0]
	v_pk_add_f32 v[118:119], v[118:119], 1.0 op_sel_hi:[1,0]
	v_pk_mul_f32 v[124:125], v[124:125], v[116:117]
	v_pk_mul_f32 v[116:117], v[116:117], v[120:121]
	v_pk_mul_f32 v[126:127], v[126:127], v[118:119]
	v_pk_mul_f32 v[118:119], v[118:119], v[122:123]
	v_rcp_f32_e32 v116, v116
	v_rcp_f32_e32 v117, v117
	v_rcp_f32_e32 v118, v118
	v_rcp_f32_e32 v119, v119
	s_waitcnt lgkmcnt(3)
	v_pk_fma_f32 v[124:125], v[172:173], v[120:121], v[124:125]
	v_pk_fma_f32 v[126:127], v[174:175], v[122:123], v[126:127]
	v_pk_mul_f32 v[116:117], v[116:117], v[124:125]
	v_pk_mul_f32 v[118:119], v[118:119], v[126:127]
	global_store_dwordx4 v[176:177], v[116:119], off sc1
	s_nop 1
	v_pk_mul_f32 v[116:117], v[116:117], s[96:97] op_sel_hi:[1,0]
	v_pk_mul_f32 v[118:119], v[118:119], s[96:97] op_sel_hi:[1,0]
	v_exp_f32_e32 v112, v112
	v_exp_f32_e32 v113, v113
	v_exp_f32_e32 v114, v114
	v_pk_fma_f32 v[112:113], v[112:113], s[98:99], s[98:99] op_sel_hi:[1,0,0]
	v_exp_f32_e32 v115, v115
	v_exp_f32_e32 v116, v116
	v_pk_fma_f32 v[114:115], v[114:115], s[98:99], s[98:99] op_sel_hi:[1,0,0]
	v_exp_f32_e32 v117, v117
	v_exp_f32_e32 v118, v118
	v_pk_add_f32 v[116:117], v[116:117], 1.0 op_sel_hi:[1,0]
	v_exp_f32_e32 v119, v119
	v_pk_mul_f32 v[112:113], v[112:113], v[116:117]
	v_rcp_f32_e32 v112, v112
	v_pk_add_f32 v[118:119], v[118:119], 1.0 op_sel_hi:[1,0]
	v_rcp_f32_e32 v113, v113
	v_pk_mul_f32 v[114:115], v[114:115], v[118:119]
	v_pk_add_f32 v[116:117], v[116:117], 2.0 op_sel_hi:[1,0] neg_lo:[1,0] neg_hi:[1,0]
	v_rcp_f32_e32 v114, v114
	v_rcp_f32_e32 v115, v115
	v_pk_add_f32 v[118:119], v[118:119], 2.0 op_sel_hi:[1,0] neg_lo:[1,0] neg_hi:[1,0]
	v_pk_mul_f32 v[112:113], v[112:113], v[116:117]
	v_pk_mul_f32 v[114:115], v[114:115], v[118:119]
	v_cvt_pk_fp8_f32 v124, v112, v113
	s_add_u32 s0, s8, s27
	s_addc_u32 s1, s9, 0
	s_ashr_i32 s35, s34, 31
	s_lshl_b64 s[34:35], s[34:35], 21
	v_ashrrev_i32_e32 v209, 31, v208
	s_add_u32 s36, s73, s34
	v_lshl_add_u64 v[122:123], s[0:1], 0, v[210:211]
	v_cvt_pk_fp8_f32 v124, v114, v115 op_sel:[0,0,1]
	v_lshlrev_b64 v[116:117], 10, v[208:209]
	s_addc_u32 s37, s74, s35
	v_lshl_add_u64 v[118:119], v[122:123], 0, v[116:117]
	global_store_dword v[118:119], v124, off
	s_cmp_eq_u32 s30, 7
	s_cselect_b64 s[34:35], -1, 0
	s_cmp_lg_u32 s30, 7
	v_lshl_add_u64 v[120:121], v[210:211], 1, s[36:37]
	v_pk_mul_f32 v[112:113], v[112:113], s[98:99] op_sel_hi:[1,0]
	v_pk_mul_f32 v[114:115], v[114:115], s[98:99] op_sel_hi:[1,0]
	v_cvt_pk_f16_f32 v112, v112, v113
	v_cvt_pk_f16_f32 v113, v114, v115
	v_lshl_add_u64 v[114:115], v[116:117], 1, v[120:121]
	global_store_dwordx2 v[114:115], v[112:113], off
	v_exp_f32_e32 v104, v104
	v_exp_f32_e32 v105, v105
	v_exp_f32_e32 v106, v106
	v_pk_add_f32 v[104:105], v[104:105], 1.0 op_sel_hi:[1,0]
	v_exp_f32_e32 v107, v107
	v_exp_f32_e32 v108, v108
	v_pk_add_f32 v[106:107], v[106:107], 1.0 op_sel_hi:[1,0]
	v_exp_f32_e32 v109, v109
	v_exp_f32_e32 v110, v110
	v_pk_add_f32 v[108:109], v[108:109], 1.0 op_sel_hi:[1,0]
	v_exp_f32_e32 v111, v111
	v_exp_f32_e32 v100, v100
	v_pk_add_f32 v[110:111], v[110:111], 1.0 op_sel_hi:[1,0]
	v_exp_f32_e32 v101, v101
	v_pk_mul_f32 v[104:105], v[104:105], v[108:109]
	v_exp_f32_e32 v102, v102
	v_pk_mul_f32 v[106:107], v[106:107], v[110:111]
	v_exp_f32_e32 v103, v103
	v_pk_add_f32 v[108:109], v[108:109], 2.0 op_sel_hi:[1,0] neg_lo:[1,0] neg_hi:[1,0]
	v_pk_add_f32 v[100:101], v[100:101], 1.0 op_sel_hi:[1,0]
	v_pk_add_f32 v[110:111], v[110:111], 2.0 op_sel_hi:[1,0] neg_lo:[1,0] neg_hi:[1,0]
	v_pk_add_f32 v[102:103], v[102:103], 1.0 op_sel_hi:[1,0]
	v_pk_mul_f32 v[108:109], v[108:109], v[100:101]
	v_pk_mul_f32 v[100:101], v[100:101], v[104:105]
	v_pk_mul_f32 v[110:111], v[110:111], v[102:103]
	v_pk_mul_f32 v[102:103], v[102:103], v[106:107]
	v_rcp_f32_e32 v100, v100
	v_rcp_f32_e32 v101, v101
	v_rcp_f32_e32 v102, v102
	v_rcp_f32_e32 v103, v103
	s_waitcnt lgkmcnt(2)
	v_pk_fma_f32 v[108:109], v[168:169], v[104:105], v[108:109]
	v_pk_fma_f32 v[110:111], v[170:171], v[106:107], v[110:111]
	v_lshl_add_u64 v[104:105], v[176:177], 0, s[18:19]
	v_pk_mul_f32 v[100:101], v[100:101], v[108:109]
	v_pk_mul_f32 v[102:103], v[102:103], v[110:111]
	global_store_dwordx4 v[104:105], v[100:103], off sc1
	s_nop 1
	v_pk_mul_f32 v[100:101], v[100:101], s[96:97] op_sel_hi:[1,0]
	v_pk_mul_f32 v[102:103], v[102:103], s[96:97] op_sel_hi:[1,0]
	v_exp_f32_e32 v96, v96
	v_exp_f32_e32 v97, v97
	v_exp_f32_e32 v98, v98
	v_pk_fma_f32 v[96:97], v[96:97], s[98:99], s[98:99] op_sel_hi:[1,0,0]
	v_exp_f32_e32 v99, v99
	v_exp_f32_e32 v100, v100
	v_pk_fma_f32 v[98:99], v[98:99], s[98:99], s[98:99] op_sel_hi:[1,0,0]
	v_exp_f32_e32 v101, v101
	v_exp_f32_e32 v102, v102
	v_pk_add_f32 v[100:101], v[100:101], 1.0 op_sel_hi:[1,0]
	v_exp_f32_e32 v103, v103
	v_pk_mul_f32 v[96:97], v[96:97], v[100:101]
	v_rcp_f32_e32 v96, v96
	v_pk_add_f32 v[102:103], v[102:103], 1.0 op_sel_hi:[1,0]
	v_rcp_f32_e32 v97, v97
	v_pk_mul_f32 v[98:99], v[98:99], v[102:103]
	v_pk_add_f32 v[100:101], v[100:101], 2.0 op_sel_hi:[1,0] neg_lo:[1,0] neg_hi:[1,0]
	v_rcp_f32_e32 v98, v98
	v_rcp_f32_e32 v99, v99
	v_pk_add_f32 v[102:103], v[102:103], 2.0 op_sel_hi:[1,0] neg_lo:[1,0] neg_hi:[1,0]
	v_pk_mul_f32 v[96:97], v[96:97], v[100:101]
	v_pk_mul_f32 v[98:99], v[98:99], v[102:103]
	v_cvt_pk_fp8_f32 v104, v96, v97
	v_ashrrev_i32_e32 v207, 31, v206
	v_lshlrev_b64 v[100:101], 10, v[206:207]
	v_lshl_add_u64 v[102:103], v[122:123], 0, v[100:101]
	v_cvt_pk_fp8_f32 v104, v98, v99 op_sel:[0,0,1]
	v_cndmask_b32_e64 v105, 0, 1, s[34:35]
	global_store_dword v[102:103], v104, off
	v_cmp_ne_u32_e64 s[0:1], 1, v105
	v_pk_mul_f32 v[96:97], v[96:97], s[98:99] op_sel_hi:[1,0]
	v_pk_mul_f32 v[98:99], v[98:99], s[98:99] op_sel_hi:[1,0]
	v_cvt_pk_f16_f32 v96, v96, v97
	v_cvt_pk_f16_f32 v97, v98, v99
	v_lshl_add_u64 v[98:99], v[100:101], 1, v[120:121]
	global_store_dwordx2 v[98:99], v[96:97], off
	v_exp_f32_e32 v88, v88
	v_exp_f32_e32 v89, v89
	v_exp_f32_e32 v90, v90
	v_pk_add_f32 v[88:89], v[88:89], 1.0 op_sel_hi:[1,0]
	v_exp_f32_e32 v91, v91
	v_exp_f32_e32 v92, v92
	v_pk_add_f32 v[90:91], v[90:91], 1.0 op_sel_hi:[1,0]
	v_exp_f32_e32 v93, v93
	v_exp_f32_e32 v94, v94
	v_pk_add_f32 v[92:93], v[92:93], 1.0 op_sel_hi:[1,0]
	v_exp_f32_e32 v95, v95
	v_exp_f32_e32 v84, v84
	v_pk_add_f32 v[94:95], v[94:95], 1.0 op_sel_hi:[1,0]
	v_exp_f32_e32 v85, v85
	v_pk_mul_f32 v[88:89], v[88:89], v[92:93]
	v_exp_f32_e32 v86, v86
	v_pk_mul_f32 v[90:91], v[90:91], v[94:95]
	v_exp_f32_e32 v87, v87
	v_pk_add_f32 v[92:93], v[92:93], 2.0 op_sel_hi:[1,0] neg_lo:[1,0] neg_hi:[1,0]
	v_pk_add_f32 v[84:85], v[84:85], 1.0 op_sel_hi:[1,0]
	v_pk_add_f32 v[94:95], v[94:95], 2.0 op_sel_hi:[1,0] neg_lo:[1,0] neg_hi:[1,0]
	v_pk_add_f32 v[86:87], v[86:87], 1.0 op_sel_hi:[1,0]
	v_pk_mul_f32 v[92:93], v[92:93], v[84:85]
	v_pk_mul_f32 v[84:85], v[84:85], v[88:89]
	v_pk_mul_f32 v[94:95], v[94:95], v[86:87]
	v_pk_mul_f32 v[86:87], v[86:87], v[90:91]
	v_rcp_f32_e32 v84, v84
	v_rcp_f32_e32 v85, v85
	v_rcp_f32_e32 v86, v86
	v_rcp_f32_e32 v87, v87
	s_waitcnt lgkmcnt(1)
	v_pk_fma_f32 v[92:93], v[164:165], v[88:89], v[92:93]
	v_pk_fma_f32 v[94:95], v[166:167], v[90:91], v[94:95]
	v_pk_mul_f32 v[84:85], v[84:85], v[92:93]
	v_pk_mul_f32 v[86:87], v[86:87], v[94:95]
	v_lshl_add_u64 v[88:89], v[176:177], 0, s[12:13]
	global_store_dwordx4 v[88:89], v[84:87], off sc1
	s_nop 1
	v_pk_mul_f32 v[84:85], v[84:85], s[96:97] op_sel_hi:[1,0]
	v_pk_mul_f32 v[86:87], v[86:87], s[96:97] op_sel_hi:[1,0]
	v_exp_f32_e32 v80, v80
	v_exp_f32_e32 v81, v81
	v_exp_f32_e32 v82, v82
	v_pk_fma_f32 v[80:81], v[80:81], s[98:99], s[98:99] op_sel_hi:[1,0,0]
	v_exp_f32_e32 v83, v83
	v_exp_f32_e32 v84, v84
	v_pk_fma_f32 v[82:83], v[82:83], s[98:99], s[98:99] op_sel_hi:[1,0,0]
	v_exp_f32_e32 v85, v85
	v_exp_f32_e32 v86, v86
	v_pk_add_f32 v[84:85], v[84:85], 1.0 op_sel_hi:[1,0]
	v_exp_f32_e32 v87, v87
	v_pk_mul_f32 v[80:81], v[80:81], v[84:85]
	v_rcp_f32_e32 v80, v80
	v_pk_add_f32 v[86:87], v[86:87], 1.0 op_sel_hi:[1,0]
	v_rcp_f32_e32 v81, v81
	v_pk_mul_f32 v[82:83], v[82:83], v[86:87]
	v_pk_add_f32 v[84:85], v[84:85], 2.0 op_sel_hi:[1,0] neg_lo:[1,0] neg_hi:[1,0]
	v_rcp_f32_e32 v82, v82
	v_rcp_f32_e32 v83, v83
	v_pk_add_f32 v[86:87], v[86:87], 2.0 op_sel_hi:[1,0] neg_lo:[1,0] neg_hi:[1,0]
	v_pk_mul_f32 v[80:81], v[80:81], v[84:85]
	v_pk_mul_f32 v[82:83], v[82:83], v[86:87]
	v_ashrrev_i32_e32 v205, 31, v204
	v_cvt_pk_fp8_f32 v88, v80, v81
	s_and_b64 vcc, exec, s[0:1]
	v_cvt_pk_fp8_f32 v88, v82, v83 op_sel:[0,0,1]
	v_lshlrev_b64 v[84:85], 10, v[204:205]
	v_lshl_add_u64 v[86:87], v[122:123], 0, v[84:85]
	global_store_dword v[86:87], v88, off
	v_pk_mul_f32 v[80:81], v[80:81], s[98:99] op_sel_hi:[1,0]
	v_pk_mul_f32 v[82:83], v[82:83], s[98:99] op_sel_hi:[1,0]
	v_cvt_pk_f16_f32 v80, v80, v81
	v_cvt_pk_f16_f32 v81, v82, v83
	v_lshl_add_u64 v[82:83], v[84:85], 1, v[120:121]
	global_store_dwordx2 v[82:83], v[80:81], off
	v_exp_f32_e32 v72, v72
	v_exp_f32_e32 v73, v73
	v_exp_f32_e32 v74, v74
	v_pk_add_f32 v[72:73], v[72:73], 1.0 op_sel_hi:[1,0]
	v_exp_f32_e32 v75, v75
	v_exp_f32_e32 v76, v76
	v_pk_add_f32 v[74:75], v[74:75], 1.0 op_sel_hi:[1,0]
	v_exp_f32_e32 v77, v77
	v_exp_f32_e32 v78, v78
	v_pk_add_f32 v[76:77], v[76:77], 1.0 op_sel_hi:[1,0]
	v_exp_f32_e32 v79, v79
	v_exp_f32_e32 v68, v68
	v_pk_add_f32 v[78:79], v[78:79], 1.0 op_sel_hi:[1,0]
	v_exp_f32_e32 v69, v69
	v_pk_mul_f32 v[72:73], v[72:73], v[76:77]
	v_exp_f32_e32 v70, v70
	v_pk_mul_f32 v[74:75], v[74:75], v[78:79]
	v_exp_f32_e32 v71, v71
	v_pk_add_f32 v[76:77], v[76:77], 2.0 op_sel_hi:[1,0] neg_lo:[1,0] neg_hi:[1,0]
	v_pk_add_f32 v[68:69], v[68:69], 1.0 op_sel_hi:[1,0]
	v_pk_add_f32 v[78:79], v[78:79], 2.0 op_sel_hi:[1,0] neg_lo:[1,0] neg_hi:[1,0]
	v_pk_add_f32 v[70:71], v[70:71], 1.0 op_sel_hi:[1,0]
	v_pk_mul_f32 v[76:77], v[76:77], v[68:69]
	v_pk_mul_f32 v[68:69], v[68:69], v[72:73]
	v_pk_mul_f32 v[78:79], v[78:79], v[70:71]
	v_pk_mul_f32 v[70:71], v[70:71], v[74:75]
	v_rcp_f32_e32 v68, v68
	v_rcp_f32_e32 v69, v69
	v_rcp_f32_e32 v70, v70
	v_rcp_f32_e32 v71, v71
	s_waitcnt lgkmcnt(0)
	v_pk_fma_f32 v[76:77], v[160:161], v[72:73], v[76:77]
	v_pk_fma_f32 v[78:79], v[162:163], v[74:75], v[78:79]
	v_lshl_add_u64 v[72:73], v[176:177], 0, s[20:21]
	v_pk_mul_f32 v[68:69], v[68:69], v[76:77]
	v_pk_mul_f32 v[70:71], v[70:71], v[78:79]
	global_store_dwordx4 v[72:73], v[68:71], off sc1
	s_nop 1
	v_pk_mul_f32 v[68:69], v[68:69], s[96:97] op_sel_hi:[1,0]
	v_pk_mul_f32 v[70:71], v[70:71], s[96:97] op_sel_hi:[1,0]
	v_exp_f32_e32 v64, v64
	v_exp_f32_e32 v65, v65
	v_exp_f32_e32 v66, v66
	v_pk_fma_f32 v[64:65], v[64:65], s[98:99], s[98:99] op_sel_hi:[1,0,0]
	v_exp_f32_e32 v67, v67
	v_exp_f32_e32 v68, v68
	v_pk_fma_f32 v[66:67], v[66:67], s[98:99], s[98:99] op_sel_hi:[1,0,0]
	v_exp_f32_e32 v69, v69
	v_exp_f32_e32 v70, v70
	v_pk_add_f32 v[68:69], v[68:69], 1.0 op_sel_hi:[1,0]
	v_exp_f32_e32 v71, v71
	v_pk_mul_f32 v[64:65], v[64:65], v[68:69]
	v_rcp_f32_e32 v64, v64
	v_pk_add_f32 v[70:71], v[70:71], 1.0 op_sel_hi:[1,0]
	v_rcp_f32_e32 v65, v65
	v_pk_mul_f32 v[66:67], v[66:67], v[70:71]
	v_pk_add_f32 v[68:69], v[68:69], 2.0 op_sel_hi:[1,0] neg_lo:[1,0] neg_hi:[1,0]
	v_rcp_f32_e32 v66, v66
	v_rcp_f32_e32 v67, v67
	v_pk_add_f32 v[70:71], v[70:71], 2.0 op_sel_hi:[1,0] neg_lo:[1,0] neg_hi:[1,0]
	v_pk_mul_f32 v[64:65], v[64:65], v[68:69]
	v_pk_mul_f32 v[66:67], v[66:67], v[70:71]
	v_ashrrev_i32_e32 v203, 31, v202
	v_cvt_pk_fp8_f32 v72, v64, v65
	s_and_b64 vcc, exec, s[0:1]
	v_cvt_pk_fp8_f32 v72, v66, v67 op_sel:[0,0,1]
	v_lshlrev_b64 v[68:69], 10, v[202:203]
	v_lshl_add_u64 v[70:71], v[122:123], 0, v[68:69]
	global_store_dword v[70:71], v72, off
	v_pk_mul_f32 v[64:65], v[64:65], s[98:99] op_sel_hi:[1,0]
	v_pk_mul_f32 v[66:67], v[66:67], s[98:99] op_sel_hi:[1,0]
	v_cvt_pk_f16_f32 v64, v64, v65
	v_cvt_pk_f16_f32 v65, v66, v67
	v_lshl_add_u64 v[66:67], v[68:69], 1, v[120:121]
	global_store_dwordx2 v[66:67], v[64:65], off
	v_exp_f32_e32 v56, v56
	v_exp_f32_e32 v57, v57
	v_exp_f32_e32 v58, v58
	v_pk_add_f32 v[56:57], v[56:57], 1.0 op_sel_hi:[1,0]
	v_exp_f32_e32 v59, v59
	v_exp_f32_e32 v60, v60
	v_pk_add_f32 v[58:59], v[58:59], 1.0 op_sel_hi:[1,0]
	v_exp_f32_e32 v61, v61
	v_exp_f32_e32 v62, v62
	v_pk_add_f32 v[60:61], v[60:61], 1.0 op_sel_hi:[1,0]
	v_exp_f32_e32 v63, v63
	v_exp_f32_e32 v52, v52
	v_pk_add_f32 v[62:63], v[62:63], 1.0 op_sel_hi:[1,0]
	v_exp_f32_e32 v53, v53
	v_pk_mul_f32 v[56:57], v[56:57], v[60:61]
	v_exp_f32_e32 v54, v54
	v_pk_mul_f32 v[58:59], v[58:59], v[62:63]
	v_exp_f32_e32 v55, v55
	v_pk_add_f32 v[60:61], v[60:61], 2.0 op_sel_hi:[1,0] neg_lo:[1,0] neg_hi:[1,0]
	v_pk_add_f32 v[52:53], v[52:53], 1.0 op_sel_hi:[1,0]
	v_pk_add_f32 v[62:63], v[62:63], 2.0 op_sel_hi:[1,0] neg_lo:[1,0] neg_hi:[1,0]
	v_pk_add_f32 v[54:55], v[54:55], 1.0 op_sel_hi:[1,0]
	v_pk_mul_f32 v[60:61], v[60:61], v[52:53]
	v_pk_mul_f32 v[52:53], v[52:53], v[56:57]
	v_pk_mul_f32 v[62:63], v[62:63], v[54:55]
	v_pk_mul_f32 v[54:55], v[54:55], v[58:59]
	v_rcp_f32_e32 v52, v52
	v_rcp_f32_e32 v53, v53
	v_rcp_f32_e32 v54, v54
	v_rcp_f32_e32 v55, v55
	s_waitcnt vmcnt(8)
	v_pk_fma_f32 v[60:61], v[156:157], v[56:57], v[60:61]
	v_pk_fma_f32 v[62:63], v[158:159], v[58:59], v[62:63]
	v_pk_mul_f32 v[52:53], v[52:53], v[60:61]
	v_pk_mul_f32 v[54:55], v[54:55], v[62:63]
	v_lshl_add_u64 v[56:57], v[176:177], 0, s[14:15]
	global_store_dwordx4 v[56:57], v[52:55], off sc1
	s_nop 1
	v_pk_mul_f32 v[52:53], v[52:53], s[96:97] op_sel_hi:[1,0]
	v_pk_mul_f32 v[54:55], v[54:55], s[96:97] op_sel_hi:[1,0]
	v_exp_f32_e32 v48, v48
	v_exp_f32_e32 v49, v49
	v_exp_f32_e32 v50, v50
	v_pk_fma_f32 v[48:49], v[48:49], s[98:99], s[98:99] op_sel_hi:[1,0,0]
	v_exp_f32_e32 v51, v51
	v_exp_f32_e32 v52, v52
	v_pk_fma_f32 v[50:51], v[50:51], s[98:99], s[98:99] op_sel_hi:[1,0,0]
	v_exp_f32_e32 v53, v53
	v_exp_f32_e32 v54, v54
	v_pk_add_f32 v[52:53], v[52:53], 1.0 op_sel_hi:[1,0]
	v_exp_f32_e32 v55, v55
	v_pk_mul_f32 v[48:49], v[48:49], v[52:53]
	v_rcp_f32_e32 v48, v48
	v_pk_add_f32 v[54:55], v[54:55], 1.0 op_sel_hi:[1,0]
	v_rcp_f32_e32 v49, v49
	v_pk_mul_f32 v[50:51], v[50:51], v[54:55]
	v_pk_add_f32 v[52:53], v[52:53], 2.0 op_sel_hi:[1,0] neg_lo:[1,0] neg_hi:[1,0]
	v_rcp_f32_e32 v50, v50
	v_rcp_f32_e32 v51, v51
	v_pk_add_f32 v[54:55], v[54:55], 2.0 op_sel_hi:[1,0] neg_lo:[1,0] neg_hi:[1,0]
	v_pk_mul_f32 v[48:49], v[48:49], v[52:53]
	v_pk_mul_f32 v[50:51], v[50:51], v[54:55]
	v_ashrrev_i32_e32 v201, 31, v200
	v_cvt_pk_fp8_f32 v56, v48, v49
	s_and_b64 vcc, exec, s[0:1]
	v_cvt_pk_fp8_f32 v56, v50, v51 op_sel:[0,0,1]
	v_lshlrev_b64 v[52:53], 10, v[200:201]
	v_lshl_add_u64 v[54:55], v[122:123], 0, v[52:53]
	global_store_dword v[54:55], v56, off
	v_pk_mul_f32 v[48:49], v[48:49], s[98:99] op_sel_hi:[1,0]
	v_pk_mul_f32 v[50:51], v[50:51], s[98:99] op_sel_hi:[1,0]
	v_cvt_pk_f16_f32 v48, v48, v49
	v_cvt_pk_f16_f32 v49, v50, v51
	v_lshl_add_u64 v[50:51], v[52:53], 1, v[120:121]
	global_store_dwordx2 v[50:51], v[48:49], off
	v_exp_f32_e32 v40, v40
	v_exp_f32_e32 v41, v41
	v_exp_f32_e32 v42, v42
	v_pk_add_f32 v[40:41], v[40:41], 1.0 op_sel_hi:[1,0]
	v_exp_f32_e32 v43, v43
	v_exp_f32_e32 v44, v44
	v_pk_add_f32 v[42:43], v[42:43], 1.0 op_sel_hi:[1,0]
	v_exp_f32_e32 v45, v45
	v_exp_f32_e32 v46, v46
	v_pk_add_f32 v[44:45], v[44:45], 1.0 op_sel_hi:[1,0]
	v_exp_f32_e32 v47, v47
	v_exp_f32_e32 v36, v36
	v_pk_add_f32 v[46:47], v[46:47], 1.0 op_sel_hi:[1,0]
	v_exp_f32_e32 v37, v37
	v_pk_mul_f32 v[40:41], v[40:41], v[44:45]
	v_exp_f32_e32 v38, v38
	v_pk_mul_f32 v[42:43], v[42:43], v[46:47]
	v_exp_f32_e32 v39, v39
	v_pk_add_f32 v[44:45], v[44:45], 2.0 op_sel_hi:[1,0] neg_lo:[1,0] neg_hi:[1,0]
	v_pk_add_f32 v[36:37], v[36:37], 1.0 op_sel_hi:[1,0]
	v_pk_add_f32 v[46:47], v[46:47], 2.0 op_sel_hi:[1,0] neg_lo:[1,0] neg_hi:[1,0]
	v_pk_add_f32 v[38:39], v[38:39], 1.0 op_sel_hi:[1,0]
	v_pk_mul_f32 v[44:45], v[44:45], v[36:37]
	v_pk_mul_f32 v[36:37], v[36:37], v[40:41]
	v_pk_mul_f32 v[46:47], v[46:47], v[38:39]
	v_pk_mul_f32 v[38:39], v[38:39], v[42:43]
	v_rcp_f32_e32 v36, v36
	v_rcp_f32_e32 v37, v37
	v_rcp_f32_e32 v38, v38
	v_rcp_f32_e32 v39, v39
	v_pk_fma_f32 v[44:45], v[152:153], v[40:41], v[44:45]
	v_pk_fma_f32 v[46:47], v[154:155], v[42:43], v[46:47]
	v_lshl_add_u64 v[40:41], v[176:177], 0, s[22:23]
	v_pk_mul_f32 v[36:37], v[36:37], v[44:45]
	v_pk_mul_f32 v[38:39], v[38:39], v[46:47]
	global_store_dwordx4 v[40:41], v[36:39], off sc1
	s_nop 1
	v_pk_mul_f32 v[36:37], v[36:37], s[96:97] op_sel_hi:[1,0]
	v_pk_mul_f32 v[38:39], v[38:39], s[96:97] op_sel_hi:[1,0]
	v_exp_f32_e32 v32, v32
	v_exp_f32_e32 v33, v33
	v_exp_f32_e32 v34, v34
	v_pk_fma_f32 v[32:33], v[32:33], s[98:99], s[98:99] op_sel_hi:[1,0,0]
	v_exp_f32_e32 v35, v35
	v_exp_f32_e32 v36, v36
	v_pk_fma_f32 v[34:35], v[34:35], s[98:99], s[98:99] op_sel_hi:[1,0,0]
	v_exp_f32_e32 v37, v37
	v_exp_f32_e32 v38, v38
	v_pk_add_f32 v[36:37], v[36:37], 1.0 op_sel_hi:[1,0]
	v_exp_f32_e32 v39, v39
	v_pk_mul_f32 v[32:33], v[32:33], v[36:37]
	v_rcp_f32_e32 v32, v32
	v_pk_add_f32 v[38:39], v[38:39], 1.0 op_sel_hi:[1,0]
	v_rcp_f32_e32 v33, v33
	v_pk_mul_f32 v[34:35], v[34:35], v[38:39]
	v_pk_add_f32 v[36:37], v[36:37], 2.0 op_sel_hi:[1,0] neg_lo:[1,0] neg_hi:[1,0]
	v_rcp_f32_e32 v34, v34
	v_rcp_f32_e32 v35, v35
	v_pk_add_f32 v[38:39], v[38:39], 2.0 op_sel_hi:[1,0] neg_lo:[1,0] neg_hi:[1,0]
	v_pk_mul_f32 v[32:33], v[32:33], v[36:37]
	v_pk_mul_f32 v[34:35], v[34:35], v[38:39]
	v_cvt_pk_fp8_f32 v40, v32, v33
	v_or_b32_e32 v36, 16, v200
	v_ashrrev_i32_e32 v37, 31, v36
	v_lshlrev_b64 v[36:37], 10, v[36:37]
	v_cvt_pk_fp8_f32 v40, v34, v35 op_sel:[0,0,1]
	v_lshl_add_u64 v[38:39], v[122:123], 0, v[36:37]
	global_store_dword v[38:39], v40, off
	v_pk_mul_f32 v[32:33], v[32:33], s[98:99] op_sel_hi:[1,0]
	v_pk_mul_f32 v[34:35], v[34:35], s[98:99] op_sel_hi:[1,0]
	v_cvt_pk_f16_f32 v32, v32, v33
	v_cvt_pk_f16_f32 v33, v34, v35
	v_lshl_add_u64 v[34:35], v[36:37], 1, v[120:121]
	global_store_dwordx2 v[34:35], v[32:33], off
	v_exp_f32_e32 v24, v24
	v_exp_f32_e32 v25, v25
	v_exp_f32_e32 v26, v26
	v_pk_add_f32 v[24:25], v[24:25], 1.0 op_sel_hi:[1,0]
	v_exp_f32_e32 v27, v27
	v_exp_f32_e32 v28, v28
	v_pk_add_f32 v[26:27], v[26:27], 1.0 op_sel_hi:[1,0]
	v_exp_f32_e32 v29, v29
	v_exp_f32_e32 v30, v30
	v_pk_add_f32 v[28:29], v[28:29], 1.0 op_sel_hi:[1,0]
	v_exp_f32_e32 v31, v31
	v_exp_f32_e32 v20, v20
	v_pk_add_f32 v[30:31], v[30:31], 1.0 op_sel_hi:[1,0]
	v_exp_f32_e32 v21, v21
	v_pk_mul_f32 v[24:25], v[24:25], v[28:29]
	v_exp_f32_e32 v22, v22
	v_pk_mul_f32 v[26:27], v[26:27], v[30:31]
	v_exp_f32_e32 v23, v23
	v_pk_add_f32 v[28:29], v[28:29], 2.0 op_sel_hi:[1,0] neg_lo:[1,0] neg_hi:[1,0]
	v_pk_add_f32 v[20:21], v[20:21], 1.0 op_sel_hi:[1,0]
	v_pk_add_f32 v[30:31], v[30:31], 2.0 op_sel_hi:[1,0] neg_lo:[1,0] neg_hi:[1,0]
	v_pk_add_f32 v[22:23], v[22:23], 1.0 op_sel_hi:[1,0]
	v_pk_mul_f32 v[28:29], v[28:29], v[20:21]
	v_pk_mul_f32 v[20:21], v[20:21], v[24:25]
	v_pk_mul_f32 v[30:31], v[30:31], v[22:23]
	v_pk_mul_f32 v[22:23], v[22:23], v[26:27]
	v_rcp_f32_e32 v20, v20
	v_rcp_f32_e32 v21, v21
	v_rcp_f32_e32 v22, v22
	v_rcp_f32_e32 v23, v23
	v_pk_fma_f32 v[28:29], v[148:149], v[24:25], v[28:29]
	v_pk_fma_f32 v[30:31], v[150:151], v[26:27], v[30:31]
	v_pk_mul_f32 v[20:21], v[20:21], v[28:29]
	v_pk_mul_f32 v[22:23], v[22:23], v[30:31]
	v_lshl_add_u64 v[24:25], v[176:177], 0, s[16:17]
	global_store_dwordx4 v[24:25], v[20:23], off sc1
	s_nop 1
	v_pk_mul_f32 v[20:21], v[20:21], s[96:97] op_sel_hi:[1,0]
	v_pk_mul_f32 v[22:23], v[22:23], s[96:97] op_sel_hi:[1,0]
	v_exp_f32_e32 v16, v16
	v_exp_f32_e32 v17, v17
	v_exp_f32_e32 v18, v18
	v_pk_fma_f32 v[16:17], v[16:17], s[98:99], s[98:99] op_sel_hi:[1,0,0]
	v_exp_f32_e32 v19, v19
	v_exp_f32_e32 v20, v20
	v_pk_fma_f32 v[18:19], v[18:19], s[98:99], s[98:99] op_sel_hi:[1,0,0]
	v_exp_f32_e32 v21, v21
	v_exp_f32_e32 v22, v22
	v_pk_add_f32 v[20:21], v[20:21], 1.0 op_sel_hi:[1,0]
	v_exp_f32_e32 v23, v23
	v_pk_mul_f32 v[16:17], v[16:17], v[20:21]
	v_rcp_f32_e32 v16, v16
	v_pk_add_f32 v[22:23], v[22:23], 1.0 op_sel_hi:[1,0]
	v_rcp_f32_e32 v17, v17
	v_pk_mul_f32 v[18:19], v[18:19], v[22:23]
	v_pk_add_f32 v[20:21], v[20:21], 2.0 op_sel_hi:[1,0] neg_lo:[1,0] neg_hi:[1,0]
	v_rcp_f32_e32 v18, v18
	v_rcp_f32_e32 v19, v19
	v_pk_add_f32 v[22:23], v[22:23], 2.0 op_sel_hi:[1,0] neg_lo:[1,0] neg_hi:[1,0]
	v_pk_mul_f32 v[16:17], v[16:17], v[20:21]
	v_pk_mul_f32 v[18:19], v[18:19], v[22:23]
	v_cvt_pk_fp8_f32 v24, v16, v17
	v_or_b32_e32 v20, 32, v200
	v_ashrrev_i32_e32 v21, 31, v20
	v_lshlrev_b64 v[20:21], 10, v[20:21]
	v_cvt_pk_fp8_f32 v24, v18, v19 op_sel:[0,0,1]
	v_lshl_add_u64 v[22:23], v[122:123], 0, v[20:21]
	global_store_dword v[22:23], v24, off
	v_pk_mul_f32 v[16:17], v[16:17], s[98:99] op_sel_hi:[1,0]
	v_pk_mul_f32 v[18:19], v[18:19], s[98:99] op_sel_hi:[1,0]
	v_cvt_pk_f16_f32 v16, v16, v17
	v_cvt_pk_f16_f32 v17, v18, v19
	v_lshl_add_u64 v[18:19], v[20:21], 1, v[120:121]
	global_store_dwordx2 v[18:19], v[16:17], off
	v_exp_f32_e32 v8, v8
	v_exp_f32_e32 v9, v9
	v_exp_f32_e32 v10, v10
	v_pk_add_f32 v[8:9], v[8:9], 1.0 op_sel_hi:[1,0]
	v_exp_f32_e32 v11, v11
	v_exp_f32_e32 v12, v12
	v_pk_add_f32 v[10:11], v[10:11], 1.0 op_sel_hi:[1,0]
	v_exp_f32_e32 v13, v13
	v_exp_f32_e32 v14, v14
	v_pk_add_f32 v[12:13], v[12:13], 1.0 op_sel_hi:[1,0]
	v_exp_f32_e32 v15, v15
	v_exp_f32_e32 v4, v4
	v_pk_add_f32 v[14:15], v[14:15], 1.0 op_sel_hi:[1,0]
	v_exp_f32_e32 v5, v5
	v_pk_mul_f32 v[8:9], v[8:9], v[12:13]
	v_exp_f32_e32 v6, v6
	v_pk_mul_f32 v[10:11], v[10:11], v[14:15]
	v_exp_f32_e32 v7, v7
	v_pk_add_f32 v[12:13], v[12:13], 2.0 op_sel_hi:[1,0] neg_lo:[1,0] neg_hi:[1,0]
	v_pk_add_f32 v[4:5], v[4:5], 1.0 op_sel_hi:[1,0]
	v_pk_add_f32 v[14:15], v[14:15], 2.0 op_sel_hi:[1,0] neg_lo:[1,0] neg_hi:[1,0]
	v_pk_add_f32 v[6:7], v[6:7], 1.0 op_sel_hi:[1,0]
	v_pk_mul_f32 v[12:13], v[12:13], v[4:5]
	v_pk_mul_f32 v[4:5], v[4:5], v[8:9]
	v_pk_mul_f32 v[14:15], v[14:15], v[6:7]
	v_pk_mul_f32 v[6:7], v[6:7], v[10:11]
	v_rcp_f32_e32 v4, v4
	v_rcp_f32_e32 v5, v5
	v_rcp_f32_e32 v6, v6
	v_rcp_f32_e32 v7, v7
	v_pk_fma_f32 v[12:13], v[144:145], v[8:9], v[12:13]
	v_pk_fma_f32 v[14:15], v[146:147], v[10:11], v[14:15]
	v_lshl_add_u64 v[8:9], v[176:177], 0, s[24:25]
	v_pk_mul_f32 v[4:5], v[4:5], v[12:13]
	v_pk_mul_f32 v[6:7], v[6:7], v[14:15]
	global_store_dwordx4 v[8:9], v[4:7], off sc1
	s_nop 1
	v_pk_mul_f32 v[4:5], v[4:5], s[96:97] op_sel_hi:[1,0]
	v_pk_mul_f32 v[6:7], v[6:7], s[96:97] op_sel_hi:[1,0]
	v_exp_f32_e32 v0, v0
	v_exp_f32_e32 v1, v1
	v_exp_f32_e32 v2, v2
	v_pk_fma_f32 v[0:1], v[0:1], s[98:99], s[98:99] op_sel_hi:[1,0,0]
	v_exp_f32_e32 v3, v3
	v_exp_f32_e32 v4, v4
	v_pk_fma_f32 v[2:3], v[2:3], s[98:99], s[98:99] op_sel_hi:[1,0,0]
	v_exp_f32_e32 v5, v5
	v_exp_f32_e32 v6, v6
	v_pk_add_f32 v[4:5], v[4:5], 1.0 op_sel_hi:[1,0]
	v_exp_f32_e32 v7, v7
	v_pk_mul_f32 v[0:1], v[0:1], v[4:5]
	v_rcp_f32_e32 v0, v0
	v_pk_add_f32 v[6:7], v[6:7], 1.0 op_sel_hi:[1,0]
	v_rcp_f32_e32 v1, v1
	v_pk_mul_f32 v[2:3], v[2:3], v[6:7]
	v_pk_add_f32 v[4:5], v[4:5], 2.0 op_sel_hi:[1,0] neg_lo:[1,0] neg_hi:[1,0]
	v_rcp_f32_e32 v2, v2
	v_rcp_f32_e32 v3, v3
	v_pk_add_f32 v[6:7], v[6:7], 2.0 op_sel_hi:[1,0] neg_lo:[1,0] neg_hi:[1,0]
	v_pk_mul_f32 v[0:1], v[0:1], v[4:5]
	v_pk_mul_f32 v[2:3], v[2:3], v[6:7]
	v_cvt_pk_fp8_f32 v8, v0, v1
	v_or_b32_e32 v4, 48, v200
	v_ashrrev_i32_e32 v5, 31, v4
	v_lshlrev_b64 v[4:5], 10, v[4:5]
	v_cvt_pk_fp8_f32 v8, v2, v3 op_sel:[0,0,1]
	v_lshl_add_u64 v[6:7], v[122:123], 0, v[4:5]
	global_store_dword v[6:7], v8, off
	v_pk_mul_f32 v[0:1], v[0:1], s[98:99] op_sel_hi:[1,0]
	v_pk_mul_f32 v[2:3], v[2:3], s[98:99] op_sel_hi:[1,0]
	v_cvt_pk_f16_f32 v0, v0, v1
	v_cvt_pk_f16_f32 v1, v2, v3
	v_lshl_add_u64 v[2:3], v[4:5], 1, v[120:121]
	global_store_dwordx2 v[2:3], v[0:1], off
	s_branch .LBB2_24
